# v33: v25 + P5 weight converter keeps two load batches in flight (gain vectors loaded one super-item ahead, counted waits at sub-item boundaries instead of vmcnt(0))
# baseline (speedup 1.0000x reference)
; __device__ __forceinline__ void cvt8_load(const Cvt8Desc& d, f32x4 (&v)[16], float& gv, int wave, int lane) {
;     const float* rowp = d.W + (size_t)(d.k0 + 8 * wave) * d.ldw;
; #pragma unroll
;     for (int i = 0; i < 8; ++i) { v[2 * i] = __builtin_nontemporal_load((const f32x4*)(rowp + d.col0a)); v[2 * i + 1] = __builtin_nontemporal_load((const f32x4*)(rowp + d.col0b)); rowp += d.ldw; }
;     const float* gp = d.g ? d.g : d.W; const float gl = gp[d.k0 + 8 * wave + (lane & 7)]; gv = d.g ? gl * W8_SCALE : W8_SCALE;
; }
; __device__ __forceinline__ void cvt8_phase(const Frame& F, const KArgs& a, const int bit, const int nb, const int s_lo, const int s_hi) {
;     ...
;     constexpr int S_WGU = NE * 8 * 8;
;     auto decode = [&](int s, int j) -> Cvt8Desc {
;         Cvt8Desc D;
;         if (s < S_WGU) { const int e = s / 64, rr = s % 64, kb4 = rr / 8, cb = rr % 8, kb = kb4 * 4 + j;
;             const int da = 4 * lane, db = 256 + 4 * lane;
;             D.W = a.in[20] + (size_t)e * DM * 2 * DFF; D.g = a.in[17]; D.ldw = 2 * DFF; D.k0 = kb * 64;
;             D.col0a = ((da & 255) < 128 ? 0 : DFF) + (cb * 2 + (da >> 8)) * 128 + (da & 127); D.col0b = ((db & 255) < 128 ? 0 : DFF) + (cb * 2 + (db >> 8)) * 128 + (db & 127);
;             D.dst = ws + WS_WGU + ((size_t)e * 2 * DFF + cb * 512) * DM + kb4 * 256; return D; }
;         s -= S_WGU;
;         { const int e = s / 32, rr = s % 32, kb4 = rr / 4, cb = rr % 4, kb = kb4 * 4 + j;
;             D.W = a.in[22] + (size_t)e * DFF * DM; D.g = nullptr; D.ldw = DM; D.k0 = kb * 64; D.col0a = cb * 512 + 4 * lane; D.col0b = cb * 512 + 256 + 4 * lane;
;             D.dst = ws + WS_WD + ((size_t)e * DM + cb * 512) * DFF + kb4 * 256; return D; }
;     };
;     f32x4 va[16], vb[16]; float ga = 1.f, gb = 1.f;
;     int sidx = s_lo + bit;
;     if (sidx < s_hi) { Cvt8Desc d0 = decode(sidx, 0); cvt8_load(d0, va, ga, wave, lane); }
.LBB0_1118:
	s_cmp_eq_u64 s[2:3], 0
	s_cselect_b64 vcc, -1, 0
	s_and_b64 s[8:9], vcc, exec
	s_cselect_b32 s3, s1, s3
	s_cselect_b32 s2, s0, s2
	s_lshl_b32 s18, s75, 3
	v_mov_b32_e32 v6, s2
	s_add_i32 s2, s6, s18
	v_mov_b32_e32 v7, s3
	s_mul_hi_i32 s3, s4, s2
	s_mul_i32 s2, s4, s2
	s_lshl_b64 s[2:3], s[2:3], 2
	s_add_u32 s0, s0, s2
	s_addc_u32 s1, s1, s3
	s_lshl_b32 s14, s4, 2
	s_add_u32 s2, s0, s14
	s_addc_u32 s3, s1, 0
	s_add_u32 s4, s2, s14
	v_and_or_b32 v130, v0, 7, s18
	s_addc_u32 s5, s3, 0
	v_add_u32_e32 v8, s6, v130
	s_add_u32 s6, s4, s14
	s_addc_u32 s7, s5, 0
	s_add_u32 s8, s6, s14
	s_addc_u32 s9, s7, 0
	s_add_u32 s10, s8, s14
	v_ashrrev_i32_e32 v9, 31, v8
	s_addc_u32 s11, s9, 0
	v_lshl_add_u64 v[6:7], v[8:9], 2, v[6:7]
	s_add_u32 s12, s10, s14
	v_ashrrev_i32_e32 v5, 31, v4
	v_ashrrev_i32_e32 v3, 31, v2
	global_load_dword v67, v[6:7], off
	global_load_dword v158, v[6:7], off offset:256
	global_load_dword v159, v[6:7], off offset:512
	global_load_dword v160, v[6:7], off offset:768
	s_addc_u32 s13, s11, 0
	v_lshlrev_b64 v[6:7], 2, v[4:5]
	v_lshlrev_b64 v[8:9], 2, v[2:3]
	v_lshl_add_u64 v[2:3], s[12:13], 0, v[6:7]
	v_lshl_add_u64 v[4:5], s[12:13], 0, v[8:9]
	global_load_dwordx4 v[26:29], v[2:3], off nt
	global_load_dwordx4 v[58:61], v[4:5], off nt
	v_lshl_add_u64 v[2:3], s[10:11], 0, v[6:7]
	v_lshl_add_u64 v[4:5], s[10:11], 0, v[8:9]
	s_add_u32 s14, s12, s14
	global_load_dwordx4 v[22:25], v[2:3], off nt
	global_load_dwordx4 v[54:57], v[4:5], off nt
	v_lshl_add_u64 v[2:3], s[8:9], 0, v[6:7]
	v_lshl_add_u64 v[4:5], s[8:9], 0, v[8:9]
	v_lshl_add_u64 v[10:11], s[6:7], 0, v[6:7]
	v_lshl_add_u64 v[12:13], s[6:7], 0, v[8:9]
	s_addc_u32 s15, s13, 0
	global_load_dwordx4 v[18:21], v[2:3], off nt
	global_load_dwordx4 v[50:53], v[4:5], off nt
	s_nop 0
	global_load_dwordx4 v[2:5], v[10:11], off nt
	global_load_dwordx4 v[34:37], v[12:13], off nt
	v_lshl_add_u64 v[10:11], s[4:5], 0, v[6:7]
	v_lshl_add_u64 v[12:13], s[4:5], 0, v[8:9]
	v_lshl_add_u64 v[30:31], s[2:3], 0, v[6:7]
	v_lshl_add_u64 v[32:33], s[2:3], 0, v[8:9]
	v_lshl_add_u64 v[72:73], s[0:1], 0, v[6:7]
	v_lshl_add_u64 v[68:69], s[14:15], 0, v[6:7]
	v_lshl_add_u64 v[70:71], s[14:15], 0, v[8:9]
	global_load_dwordx4 v[14:17], v[10:11], off nt
	global_load_dwordx4 v[46:49], v[12:13], off nt
	s_nop 0
	global_load_dwordx4 v[10:13], v[30:31], off nt
	global_load_dwordx4 v[42:45], v[32:33], off nt
	v_lshl_add_u64 v[74:75], s[0:1], 0, v[8:9]
	global_load_dwordx4 v[6:9], v[72:73], off nt
	global_load_dwordx4 v[38:41], v[74:75], off nt
	global_load_dwordx4 v[30:33], v[68:69], off nt
	global_load_dwordx4 v[62:65], v[70:71], off nt
	s_and_b32 s2, s18, 16
	v_and_b32_e32 v68, 4, v0
	s_and_b32 s4, s75, 28
	s_xor_b32 s3, s2, 16
	v_or_b32_e32 v135, 0x100, v1
	s_movk_i32 s0, 0x7c
	v_mov_b32_e32 v70, s2
	v_mov_b32_e32 v71, s3
	v_cmp_eq_u32_e64 s[2:3], 0, v68
	s_xor_b32 s4, s4, 16
	v_and_or_b32 v136, v1, s0, v66
	s_lshl_b32 s0, s75, 12
	s_add_i32 s5, s75, 8
	v_cndmask_b32_e64 v137, v71, v70, s[2:3]
	v_cndmask_b32_e64 v138, v70, v71, s[2:3]
	v_xor_b32_e32 v70, s4, v1
	v_xor_b32_e32 v71, s4, v135
	s_add_i32 s4, s75, 24
	s_add_u32 s20, s72, 0xaa100000
	s_addc_u32 s21, s73, 0
	v_mov_b32_e32 v134, 0x42800000
	s_add_u32 s22, s72, 0x8a100000
	v_lshlrev_b32_e32 v76, 1, v0
	v_bitop3_b32 v69, s75, v1, 28 bitop3:0x6c
	v_bitop3_b32 v66, s75, v135, 28 bitop3:0x6c
	v_bitop3_b32 v68, s5, v135, 28 bitop3:0x6c
	s_addc_u32 s23, s73, 0
	v_and_b32_e32 v74, 15, v0
	v_bfe_u32 v75, v0, 2, 2
	v_and_b32_e32 v76, 6, v76
	s_add_i32 s0, s0, 0
	v_bitop3_b32 v72, s4, v1, 28 bitop3:0x6c
	v_bitop3_b32 v73, s4, v135, 28 bitop3:0x6c
	v_lshrrev_b32_e32 v139, 4, v0
	v_lshl_or_b32 v140, v75, 3, v76
	v_lshlrev_b32_e32 v75, 15, v75
	v_lshlrev_b32_e32 v76, 12, v76
	v_lshlrev_b32_e32 v74, 4, v74
	v_lshl_add_u32 v141, v69, 3, s0
	v_lshl_add_u32 v142, v66, 3, s0
	v_lshl_add_u32 v144, v68, 3, s0
	s_add_i32 s4, s0, 0x10000
	v_mov_b32_e32 v131, 0
	s_mov_b32 s1, 0
	s_mov_b32 s24, 0x10000
	v_lshl_add_u32 v145, v70, 3, s4
	v_lshl_add_u32 v146, v71, 3, s4
	v_or_b32_e32 v149, 0x80, v136
	v_add3_u32 v150, 0, v75, v76
	v_lshl_or_b32 v132, v139, 11, v74
	v_mov_b32_e32 v133, v131
	s_waitcnt vmcnt(16)
	v_mul_f32_e32 v67, 0x42800000, v67
	v_cndmask_b32_e32 v153, v67, v134, vcc
	v_bitop3_b32 v67, s5, v1, 28 bitop3:0x6c
	v_lshl_add_u32 v143, v67, 3, s0
	s_add_i32 s0, s0, 0x18000
	v_lshl_add_u32 v147, v72, 3, s0
	v_lshl_add_u32 v148, v73, 3, s0
	s_mov_b32 s25, 0xc3e00000
	s_mov_b32 s26, 0x20000
	s_mov_b32 s27, 0x30000
	v_mov_b32_e32 v151, 0x43e00000

; #define LAS __attribute__((address_space(3)))
; __device__ __forceinline__ void cvt8_load(const Cvt8Desc& d, f32x4 (&v)[16], float& gv, int wave, int lane) {
;     const float* rowp = d.W + (size_t)(d.k0 + 8 * wave) * d.ldw;
; #pragma unroll
;     for (int i = 0; i < 8; ++i) { v[2 * i] = __builtin_nontemporal_load((const f32x4*)(rowp + d.col0a)); v[2 * i + 1] = __builtin_nontemporal_load((const f32x4*)(rowp + d.col0b)); rowp += d.ldw; }
;     const float* gp = d.g ? d.g : d.W; const float gl = gp[d.k0 + 8 * wave + (lane & 7)]; gv = d.g ? gl * W8_SCALE : W8_SCALE;
; }
; __device__ __forceinline__ void cvt8_pack(f32x4 (&v)[16], float gv, LAS unsigned char* lds, int sub, int wave, int lane) {
;     float gs[8];
; #pragma unroll
;     for (int i = 0; i < 8; ++i) gs[i] = __builtin_bit_cast(float, __builtin_amdgcn_readlane(__builtin_bit_cast(int, gv), i));
; #pragma unroll
;     for (int hf = 0; hf < 2; ++hf) { u32x4 w[2];
; #pragma unroll
;         for (int j = 0; j < 4; ++j) { const unsigned lo = pk4_fp8(v[0 + hf][j] * gs[0], v[2 + hf][j] * gs[1], v[4 + hf][j] * gs[2], v[6 + hf][j] * gs[3]), hi = pk4_fp8(v[8 + hf][j] * gs[4], v[10 + hf][j] * gs[5], v[12 + hf][j] * gs[6], v[14 + hf][j] * gs[7]);
;             if (j & 1) { w[j >> 1].z = lo; w[j >> 1].w = hi; } else { w[j >> 1].x = lo; w[j >> 1].y = hi; } }
;         const int sw = 8 * sub + 2 * (wave >> 1);
;         LAS unsigned char* p = lds + sub * 32768 + wave * 4096 + ((hf * 256 + 4 * lane) ^ (sw & 28)) * 8;
;         { const int o0 = 8 * (sw & 2), o1 = 16 - o0; const bool q = (lane >> 2) & 1;
;           *(LAS u32x4*)(p + (q ? o1 : o0)) = q ? w[1] : w[0]; *(LAS u32x4*)(p + (q ? o0 : o1)) = q ? w[0] : w[1]; } }
; __device__ __forceinline__ void cvt8_phase(const Frame& F, const KArgs& a, const int bit, const int nb, const int s_lo, const int s_hi) {
;     ...
;     while (sidx < s_hi) {
;         const int snext = sidx + nb; const bool more = snext < s_hi;
;         { Cvt8Desc d1 = decode(sidx, 1); cvt8_load(d1, vb, gb, wave, lane); } cvt8_pack(va, ga, F.lds, 0, wave, lane);
;         { Cvt8Desc d2 = decode(sidx, 2); cvt8_load(d2, va, ga, wave, lane); } cvt8_pack(vb, gb, F.lds, 1, wave, lane);
.LBB0_1123:
	s_add_i32 s0, s18, s10
	s_add_i32 s0, s0, 64
	s_mul_hi_i32 s15, s4, s0
	s_mul_i32 s14, s4, s0
	s_lshl_b64 s[14:15], s[14:15], 2
	s_add_u32 s14, s12, s14
	s_addc_u32 s15, s13, s15
	s_lshl_b32 s0, s4, 2
	v_ashrrev_i32_e32 v69, 31, v68
	v_ashrrev_i32_e32 v67, 31, v66
	s_add_u32 s4, s14, s0
	v_lshlrev_b64 v[94:95], 2, v[68:69]
	v_lshlrev_b64 v[96:97], 2, v[66:67]
	s_addc_u32 s5, s15, 0
	v_lshl_add_u64 v[70:71], s[4:5], 0, v[94:95]
	v_lshl_add_u64 v[72:73], s[4:5], 0, v[96:97]
	s_add_u32 s4, s4, s0
	s_addc_u32 s5, s5, 0
	v_lshl_add_u64 v[74:75], s[4:5], 0, v[94:95]
	v_lshl_add_u64 v[76:77], s[4:5], 0, v[96:97]
	s_add_u32 s4, s4, s0
	v_lshl_add_u64 v[68:69], s[14:15], 0, v[94:95]
	v_lshl_add_u64 v[66:67], s[14:15], 0, v[96:97]
	s_addc_u32 s5, s5, 0
	global_load_dwordx4 v[98:101], v[68:69], off nt
	s_nop 0
	global_load_dwordx4 v[66:69], v[66:67], off nt
	s_nop 0
	global_load_dwordx4 v[102:105], v[70:71], off nt
	s_nop 0
	global_load_dwordx4 v[70:73], v[72:73], off nt
	s_nop 0
	global_load_dwordx4 v[110:113], v[74:75], off nt
	global_load_dwordx4 v[78:81], v[76:77], off nt
	v_lshl_add_u64 v[74:75], s[4:5], 0, v[94:95]
	v_lshl_add_u64 v[76:77], s[4:5], 0, v[96:97]
	s_add_u32 s4, s4, s0
	s_addc_u32 s5, s5, 0
	v_lshl_add_u64 v[82:83], s[4:5], 0, v[94:95]
	v_lshl_add_u64 v[84:85], s[4:5], 0, v[96:97]
	s_add_u32 s4, s4, s0
	s_addc_u32 s5, s5, 0
	v_lshl_add_u64 v[86:87], s[4:5], 0, v[94:95]
	v_lshl_add_u64 v[88:89], s[4:5], 0, v[96:97]
	s_add_u32 s4, s4, s0
	s_addc_u32 s5, s5, 0
	v_lshl_add_u64 v[90:91], s[4:5], 0, v[94:95]
	v_lshl_add_u64 v[92:93], s[4:5], 0, v[96:97]
	s_add_u32 s4, s4, s0
	s_addc_u32 s5, s5, 0
	s_cmp_eq_u64 s[8:9], 0
	v_lshl_add_u64 v[94:95], s[4:5], 0, v[94:95]
	v_lshl_add_u64 v[96:97], s[4:5], 0, v[96:97]
	s_cselect_b64 s[4:5], -1, 0
	s_and_b64 s[14:15], s[4:5], exec
	s_cselect_b32 s0, s13, s9
	s_cselect_b32 s8, s12, s8
	s_ashr_i32 s11, s10, 31
	v_lshl_add_u64 v[156:157], s[10:11], 0, v[130:131]
	v_readlane_b32 s12, v153, 4
	v_readlane_b32 s11, v153, 5
	v_mov_b32_e32 v154, s8
	s_waitcnt vmcnt(16)
	v_mul_f32_e32 v50, s12, v50
	v_mul_f32_e32 v54, s11, v54
	v_mov_b32_e32 v155, s0
	v_readlane_b32 s9, v153, 0
	v_readlane_b32 s8, v153, 1
	v_readlane_b32 s10, v153, 2
	v_readlane_b32 s0, v153, 3
	v_readlane_b32 s14, v153, 6
	v_readlane_b32 s13, v153, 7
	v_med3_f32 v50, v50, s25, v151
	v_med3_f32 v54, v54, s25, v151
	v_mov_b32_e32 v153, 0
	v_cvt_pk_fp8_f32 v153, v50, v54
	v_mul_f32_e32 v58, s14, v58
	s_waitcnt vmcnt(6)
	v_mul_f32_e32 v54, s13, v62
	v_med3_f32 v50, v58, s25, v151
	v_med3_f32 v54, v54, s25, v151
	v_mul_f32_e32 v38, s9, v38
	v_mul_f32_e32 v42, s8, v42
	v_cvt_pk_fp8_f32 v153, v50, v54 op_sel:[0,0,1]
	v_med3_f32 v38, v38, s25, v151
	v_med3_f32 v42, v42, s25, v151
	v_mov_b32_e32 v50, 0
	v_cvt_pk_fp8_f32 v50, v38, v42
	v_lshl_add_u64 v[154:155], v[156:157], 2, v[154:155]
	global_load_dwordx4 v[106:109], v[74:75], off nt
	s_nop 0
	global_load_dwordx4 v[74:77], v[76:77], off nt
	s_nop 0
	global_load_dwordx4 v[114:117], v[82:83], off nt
	s_nop 0
	global_load_dwordx4 v[82:85], v[84:85], off nt
	s_nop 0
	global_load_dwordx4 v[118:121], v[86:87], off nt
	s_nop 0
	global_load_dwordx4 v[86:89], v[88:89], off nt
	s_nop 0
	global_load_dwordx4 v[126:129], v[90:91], off nt
	s_nop 0
	global_load_dwordx4 v[90:93], v[92:93], off nt
	s_nop 0
	global_load_dwordx4 v[122:125], v[94:95], off nt
	s_nop 0
	global_load_dwordx4 v[94:97], v[96:97], off nt
	v_mul_f32_e32 v46, s10, v46
	v_mul_f32_e32 v34, s0, v34
	v_med3_f32 v38, v46, s25, v151
	v_med3_f32 v34, v34, s25, v151
	v_cvt_pk_fp8_f32 v50, v38, v34 op_sel:[0,0,1]
	v_mul_f32_e32 v38, s12, v51
	v_mul_f32_e32 v42, s11, v55
	v_med3_f32 v38, v38, s25, v151
	v_med3_f32 v42, v42, s25, v151
	v_mov_b32_e32 v46, 0
	v_cvt_pk_fp8_f32 v46, v38, v42
	v_mul_f32_e32 v34, s14, v59
	v_mul_f32_e32 v38, s13, v63
	v_med3_f32 v34, v34, s25, v151
	v_med3_f32 v38, v38, s25, v151
	v_cvt_pk_fp8_f32 v46, v34, v38 op_sel:[0,0,1]
	v_mul_f32_e32 v38, s9, v39
	v_mul_f32_e32 v39, s8, v43
	v_med3_f32 v38, v38, s25, v151
	v_med3_f32 v39, v39, s25, v151
	v_mov_b32_e32 v42, 0
	v_cvt_pk_fp8_f32 v42, v38, v39
	v_mul_f32_e32 v34, s10, v47
	v_mul_f32_e32 v35, s0, v35
	v_med3_f32 v34, v34, s25, v151
	v_med3_f32 v35, v35, s25, v151
	v_cvt_pk_fp8_f32 v42, v34, v35 op_sel:[0,0,1]
	v_mul_f32_e32 v35, s12, v52
	v_mul_f32_e32 v38, s11, v56
	v_med3_f32 v35, v35, s25, v151
	v_med3_f32 v38, v38, s25, v151
	v_mov_b32_e32 v39, 0
	v_cvt_pk_fp8_f32 v39, v35, v38
	v_mul_f32_e32 v34, s14, v60
	v_mul_f32_e32 v35, s13, v64
	v_med3_f32 v34, v34, s25, v151
	v_med3_f32 v35, v35, s25, v151
	v_cvt_pk_fp8_f32 v39, v34, v35 op_sel:[0,0,1]
	v_mul_f32_e32 v35, s0, v36
	v_mul_f32_e32 v36, s9, v40
	v_mul_f32_e32 v38, s8, v44
	v_med3_f32 v36, v36, s25, v151
	v_med3_f32 v38, v38, s25, v151
	v_mov_b32_e32 v40, 0
	v_cvt_pk_fp8_f32 v40, v36, v38
	v_mul_f32_e32 v38, s12, v53
	v_mul_f32_e32 v43, s11, v57
	v_med3_f32 v38, v38, s25, v151
	v_med3_f32 v43, v43, s25, v151
	v_mov_b32_e32 v44, 0
	v_cvt_pk_fp8_f32 v44, v38, v43
	v_mul_f32_e32 v36, s14, v61
	v_mul_f32_e32 v38, s13, v65
; #define LAS __attribute__((address_space(3)))
; __device__ __forceinline__ void cvt8_pack(f32x4 (&v)[16], float gv, LAS unsigned char* lds, int sub, int wave, int lane) {
;     float gs[8];
; #pragma unroll
;     for (int i = 0; i < 8; ++i) gs[i] = __builtin_bit_cast(float, __builtin_amdgcn_readlane(__builtin_bit_cast(int, gv), i));
; #pragma unroll
;     for (int hf = 0; hf < 2; ++hf) { u32x4 w[2];
; #pragma unroll
;         for (int j = 0; j < 4; ++j) { const unsigned lo = pk4_fp8(v[0 + hf][j] * gs[0], v[2 + hf][j] * gs[1], v[4 + hf][j] * gs[2], v[6 + hf][j] * gs[3]), hi = pk4_fp8(v[8 + hf][j] * gs[4], v[10 + hf][j] * gs[5], v[12 + hf][j] * gs[6], v[14 + hf][j] * gs[7]);
;             if (j & 1) { w[j >> 1].z = lo; w[j >> 1].w = hi; } else { w[j >> 1].x = lo; w[j >> 1].y = hi; } }
;         const int sw = 8 * sub + 2 * (wave >> 1);
;         LAS unsigned char* p = lds + sub * 32768 + wave * 4096 + ((hf * 256 + 4 * lane) ^ (sw & 28)) * 8;
;         { const int o0 = 8 * (sw & 2), o1 = 16 - o0; const bool q = (lane >> 2) & 1;
;           *(LAS u32x4*)(p + (q ? o1 : o0)) = q ? w[1] : w[0]; *(LAS u32x4*)(p + (q ? o0 : o1)) = q ? w[0] : w[1]; } }
; __device__ __forceinline__ void cvt8_phase(const Frame& F, const KArgs& a, const int bit, const int nb, const int s_lo, const int s_hi) {
;     ...
;     while (sidx < s_hi) {
;         const int snext = sidx + nb; const bool more = snext < s_hi;
;         { Cvt8Desc d1 = decode(sidx, 1); cvt8_load(d1, vb, gb, wave, lane); } cvt8_pack(va, ga, F.lds, 0, wave, lane);
;         { Cvt8Desc d2 = decode(sidx, 2); cvt8_load(d2, va, ga, wave, lane); } cvt8_pack(vb, gb, F.lds, 1, wave, lane);
;         { Cvt8Desc d3 = decode(sidx, 3); cvt8_load(d3, vb, gb, wave, lane); } cvt8_pack(va, ga, F.lds, 2, wave, lane);
;         { Cvt8Desc dn = decode(more ? snext : sidx, 0); cvt8_load(dn, va, ga, wave, lane); } cvt8_pack(vb, gb, F.lds, 3, wave, lane);
;         cvt8_flush(decode(sidx, 0).dst, F.lds, tid);
	v_med3_f32 v36, v36, s25, v151
	v_med3_f32 v38, v38, s25, v151
	v_cvt_pk_fp8_f32 v44, v36, v38 op_sel:[0,0,1]
	v_mul_f32_e32 v38, s9, v41
	v_mul_f32_e32 v41, s8, v45
	v_med3_f32 v38, v38, s25, v151
	v_med3_f32 v41, v41, s25, v151
	v_mov_b32_e32 v43, 0
	v_cvt_pk_fp8_f32 v43, v38, v41
	v_mul_f32_e32 v34, s10, v48
	v_mul_f32_e32 v36, s10, v49
	v_mul_f32_e32 v37, s0, v37
	v_med3_f32 v34, v34, s25, v151
	v_med3_f32 v36, v36, s25, v151
	v_med3_f32 v37, v37, s25, v151
	v_med3_f32 v35, v35, s25, v151
	v_cvt_pk_fp8_f32 v43, v36, v37 op_sel:[0,0,1]
	v_cvt_pk_fp8_f32 v40, v34, v35 op_sel:[0,0,1]
	v_cndmask_b32_e64 v37, v44, v46, s[2:3]
	v_cndmask_b32_e64 v35, v39, v153, s[2:3]
	v_cndmask_b32_e64 v36, v43, v42, s[2:3]
	v_cndmask_b32_e64 v34, v40, v50, s[2:3]
	v_add_u32_e32 v38, v141, v137
	ds_write_b128 v38, v[34:37]
	v_cndmask_b32_e64 v37, v46, v44, s[2:3]
	v_cndmask_b32_e64 v36, v42, v43, s[2:3]
	v_cndmask_b32_e64 v35, v153, v39, s[2:3]
	v_cndmask_b32_e64 v34, v50, v40, s[2:3]
	v_add_u32_e32 v38, v141, v138
	v_mul_f32_e32 v21, s12, v21
	v_mul_f32_e32 v25, s11, v25
	ds_write_b128 v38, v[34:37]
	v_med3_f32 v21, v21, s25, v151
	v_med3_f32 v25, v25, s25, v151
	v_mov_b32_e32 v34, 0
	v_cvt_pk_fp8_f32 v34, v21, v25
	v_mul_f32_e32 v29, s14, v29
	v_mul_f32_e32 v25, s13, v33
	v_med3_f32 v21, v29, s25, v151
	v_med3_f32 v25, v25, s25, v151
	v_mul_f32_e32 v6, s9, v6
	v_mul_f32_e32 v10, s8, v10
	v_cvt_pk_fp8_f32 v34, v21, v25 op_sel:[0,0,1]
	v_med3_f32 v6, v6, s25, v151
	v_med3_f32 v10, v10, s25, v151
	v_mov_b32_e32 v21, 0
	v_cvt_pk_fp8_f32 v21, v6, v10
	v_mul_f32_e32 v14, s10, v14
	v_mul_f32_e32 v2, s0, v2
	v_med3_f32 v6, v14, s25, v151
	v_med3_f32 v2, v2, s25, v151
	v_cvt_pk_fp8_f32 v21, v6, v2 op_sel:[0,0,1]
	v_mul_f32_e32 v6, s12, v18
	v_mul_f32_e32 v10, s11, v22
	v_med3_f32 v6, v6, s25, v151
	v_med3_f32 v10, v10, s25, v151
	v_mov_b32_e32 v14, 0
	v_cvt_pk_fp8_f32 v14, v6, v10
	v_mul_f32_e32 v2, s14, v26
	v_mul_f32_e32 v6, s13, v30
	v_med3_f32 v2, v2, s25, v151
	v_med3_f32 v6, v6, s25, v151
	v_cvt_pk_fp8_f32 v14, v2, v6 op_sel:[0,0,1]
	v_mul_f32_e32 v6, s9, v7
	v_mul_f32_e32 v7, s8, v11
	v_med3_f32 v6, v6, s25, v151
	v_med3_f32 v7, v7, s25, v151
	v_mov_b32_e32 v10, 0
	v_cvt_pk_fp8_f32 v10, v6, v7
	v_mul_f32_e32 v2, s10, v15
	v_mul_f32_e32 v3, s0, v3
	v_med3_f32 v2, v2, s25, v151
	v_med3_f32 v3, v3, s25, v151
	v_cvt_pk_fp8_f32 v10, v2, v3 op_sel:[0,0,1]
	v_mul_f32_e32 v3, s12, v19
	v_mul_f32_e32 v6, s11, v23
	v_med3_f32 v3, v3, s25, v151
	v_med3_f32 v6, v6, s25, v151
	v_mov_b32_e32 v7, 0
	v_cvt_pk_fp8_f32 v7, v3, v6
	v_mul_f32_e32 v2, s14, v27
	v_mul_f32_e32 v3, s13, v31
	v_mul_f32_e32 v6, s8, v12
	v_mul_f32_e32 v11, s12, v20
	v_mul_f32_e32 v12, s11, v24
	v_med3_f32 v2, v2, s25, v151
	v_med3_f32 v3, v3, s25, v151
	v_med3_f32 v11, v11, s25, v151
	v_med3_f32 v12, v12, s25, v151
	v_mov_b32_e32 v15, 0
	v_cvt_pk_fp8_f32 v7, v2, v3 op_sel:[0,0,1]
	v_mul_f32_e32 v3, s0, v4
	v_mul_f32_e32 v4, s9, v8
	v_cvt_pk_fp8_f32 v15, v11, v12
	v_mul_f32_e32 v9, s9, v9
	v_mul_f32_e32 v12, s8, v13
	v_med3_f32 v4, v4, s25, v151
	v_med3_f32 v6, v6, s25, v151
	v_mov_b32_e32 v8, 0
	v_med3_f32 v9, v9, s25, v151
	v_med3_f32 v12, v12, s25, v151
	v_mov_b32_e32 v13, 0
	v_cvt_pk_fp8_f32 v8, v4, v6
	v_cvt_pk_fp8_f32 v13, v9, v12
	v_mul_f32_e32 v2, s10, v16
	v_mul_f32_e32 v4, s14, v28
	v_mul_f32_e32 v6, s13, v32
	v_mul_f32_e32 v11, s10, v17
	v_mul_f32_e32 v5, s0, v5
	v_med3_f32 v2, v2, s25, v151
	v_med3_f32 v3, v3, s25, v151
	v_med3_f32 v4, v4, s25, v151
	v_med3_f32 v6, v6, s25, v151
	v_med3_f32 v9, v11, s25, v151
	v_med3_f32 v5, v5, s25, v151
	v_cvt_pk_fp8_f32 v13, v9, v5 op_sel:[0,0,1]
	v_cvt_pk_fp8_f32 v15, v4, v6 op_sel:[0,0,1]
	v_cvt_pk_fp8_f32 v8, v2, v3 op_sel:[0,0,1]
	v_cndmask_b32_e64 v5, v34, v7, s[2:3]
	v_cndmask_b32_e64 v4, v13, v10, s[2:3]
	v_cndmask_b32_e64 v3, v15, v14, s[2:3]
	v_cndmask_b32_e64 v2, v8, v21, s[2:3]
	v_add_u32_e32 v6, v142, v137
	ds_write_b128 v6, v[2:5]
	v_cndmask_b32_e64 v5, v7, v34, s[2:3]
	v_cndmask_b32_e64 v4, v10, v13, s[2:3]
	v_cndmask_b32_e64 v3, v14, v15, s[2:3]
	v_cndmask_b32_e64 v2, v21, v8, s[2:3]
	v_add_u32_e32 v6, v142, v138
	s_and_b64 vcc, exec, s[6:7]
	v_readfirstlane_b32 s10, v0
	ds_write_b128 v6, v[2:5]
	s_cbranch_vccz .LBB0_1125
	s_add_i32 s0, s19, 0xfffff800
	s_lshr_b32 s0, s0, 5
	v_readlane_b32 s36, v252, 22
	s_lshl_b64 s[8:9], s[0:1], 24
	v_readlane_b32 s48, v252, 34
	v_readlane_b32 s49, v252, 35
	s_add_u32 s12, s48, s8
	s_addc_u32 s13, s49, s9
	s_lshl_b32 s0, s19, 6
	s_and_b32 s10, s0, 0x700
	s_lshl_b32 s0, s19, 9
	s_and_b32 s0, s0, 0x600
	v_readlane_b32 s37, v252, 23
	v_readlane_b32 s38, v252, 24
	v_readlane_b32 s39, v252, 25
	v_readlane_b32 s40, v252, 26
	v_readlane_b32 s41, v252, 27
	v_readlane_b32 s42, v252, 28
	v_readlane_b32 s43, v252, 29
	v_readlane_b32 s44, v252, 30
	v_readlane_b32 s45, v252, 31
	v_readlane_b32 s46, v252, 32
	v_readlane_b32 s47, v252, 33
	v_readlane_b32 s50, v252, 36
	v_readlane_b32 s51, v252, 37
	v_or_b32_e32 v4, s0, v1
	v_or_b32_e32 v2, s0, v135
	s_mov_b64 s[8:9], 0
	s_mov_b64 s[14:15], 0x800
	s_cbranch_execz .LBB0_1126
	s_branch .LBB0_1127

; __device__ __forceinline__ void cvt8_load(const Cvt8Desc& d, f32x4 (&v)[16], float& gv, int wave, int lane) {
;     const float* rowp = d.W + (size_t)(d.k0 + 8 * wave) * d.ldw;
; #pragma unroll
;     for (int i = 0; i < 8; ++i) { v[2 * i] = __builtin_nontemporal_load((const f32x4*)(rowp + d.col0a)); v[2 * i + 1] = __builtin_nontemporal_load((const f32x4*)(rowp + d.col0b)); rowp += d.ldw; }
;     const float* gp = d.g ? d.g : d.W; const float gl = gp[d.k0 + 8 * wave + (lane & 7)]; gv = d.g ? gl * W8_SCALE : W8_SCALE;
; }
; __device__ __forceinline__ void cvt8_pack(f32x4 (&v)[16], float gv, LAS unsigned char* lds, int sub, int wave, int lane) {
;     float gs[8];
; #pragma unroll
;     for (int i = 0; i < 8; ++i) gs[i] = __builtin_bit_cast(float, __builtin_amdgcn_readlane(__builtin_bit_cast(int, gv), i));
; #pragma unroll
;     for (int hf = 0; hf < 2; ++hf) { u32x4 w[2];
; #pragma unroll
;         for (int j = 0; j < 4; ++j) { const unsigned lo = pk4_fp8(v[0 + hf][j] * gs[0], v[2 + hf][j] * gs[1], v[4 + hf][j] * gs[2], v[6 + hf][j] * gs[3]), hi = pk4_fp8(v[8 + hf][j] * gs[4], v[10 + hf][j] * gs[5], v[12 + hf][j] * gs[6], v[14 + hf][j] * gs[7]);
;             if (j & 1) { w[j >> 1].z = lo; w[j >> 1].w = hi; } else { w[j >> 1].x = lo; w[j >> 1].y = hi; } }
;         const int sw = 8 * sub + 2 * (wave >> 1);
;         LAS unsigned char* p = lds + sub * 32768 + wave * 4096 + ((hf * 256 + 4 * lane) ^ (sw & 28)) * 8;
;         { const int o0 = 8 * (sw & 2), o1 = 16 - o0; const bool q = (lane >> 2) & 1;
;           *(LAS u32x4*)(p + (q ? o1 : o0)) = q ? w[1] : w[0]; *(LAS u32x4*)(p + (q ? o0 : o1)) = q ? w[0] : w[1]; } }
; }
; __device__ __forceinline__ void cvt8_phase(const Frame& F, const KArgs& a, const int bit, const int nb, const int s_lo, const int s_hi) {
;     ...
;     while (sidx < s_hi) {
;         const int snext = sidx + nb; const bool more = snext < s_hi;
;         { Cvt8Desc d1 = decode(sidx, 1); cvt8_load(d1, vb, gb, wave, lane); } cvt8_pack(va, ga, F.lds, 0, wave, lane);
;         { Cvt8Desc d2 = decode(sidx, 2); cvt8_load(d2, va, ga, wave, lane); } cvt8_pack(vb, gb, F.lds, 1, wave, lane);
;         { Cvt8Desc d3 = decode(sidx, 3); cvt8_load(d3, vb, gb, wave, lane); } cvt8_pack(va, ga, F.lds, 2, wave, lane);
;         { Cvt8Desc dn = decode(more ? snext : sidx, 0); cvt8_load(dn, va, ga, wave, lane); } cvt8_pack(vb, gb, F.lds, 3, wave, lane);
.LBB0_1127:
	s_add_i32 s0, s18, s10
	v_mul_f32_e32 v3, 0x42800000, v158
	s_addk_i32 s0, 0x80
	v_cndmask_b32_e64 v156, v3, v134, s[4:5]
	s_mul_hi_i32 s5, s14, s0
	s_mul_i32 s4, s14, s0
	s_lshl_b64 s[4:5], s[4:5], 2
	s_add_u32 s4, s12, s4
	v_ashrrev_i32_e32 v5, 31, v4
	v_ashrrev_i32_e32 v3, 31, v2
	s_addc_u32 s5, s13, s5
	v_lshlrev_b64 v[30:31], 2, v[4:5]
	v_lshlrev_b64 v[32:33], 2, v[2:3]
	s_lshl_b32 s0, s14, 2
	v_lshl_add_u64 v[4:5], s[4:5], 0, v[30:31]
	v_lshl_add_u64 v[2:3], s[4:5], 0, v[32:33]
	s_add_u32 s4, s4, s0
	s_addc_u32 s5, s5, 0
	v_lshl_add_u64 v[6:7], s[4:5], 0, v[30:31]
	v_lshl_add_u64 v[8:9], s[4:5], 0, v[32:33]
	s_add_u32 s4, s4, s0
	s_addc_u32 s5, s5, 0
	v_lshl_add_u64 v[10:11], s[4:5], 0, v[30:31]
	v_lshl_add_u64 v[12:13], s[4:5], 0, v[32:33]
	s_add_u32 s4, s4, s0
	s_addc_u32 s5, s5, 0
	global_load_dwordx4 v[34:37], v[4:5], off nt
	s_nop 0
	global_load_dwordx4 v[2:5], v[2:3], off nt
	s_nop 0
	global_load_dwordx4 v[38:41], v[6:7], off nt
	s_nop 0
	global_load_dwordx4 v[6:9], v[8:9], off nt
	s_nop 0
	global_load_dwordx4 v[46:49], v[10:11], off nt
	global_load_dwordx4 v[14:17], v[12:13], off nt
	v_lshl_add_u64 v[10:11], s[4:5], 0, v[30:31]
	v_lshl_add_u64 v[12:13], s[4:5], 0, v[32:33]
	s_add_u32 s4, s4, s0
	s_addc_u32 s5, s5, 0
	v_lshl_add_u64 v[18:19], s[4:5], 0, v[30:31]
	v_lshl_add_u64 v[20:21], s[4:5], 0, v[32:33]
	s_add_u32 s4, s4, s0
	s_addc_u32 s5, s5, 0
	v_lshl_add_u64 v[22:23], s[4:5], 0, v[30:31]
	v_lshl_add_u64 v[24:25], s[4:5], 0, v[32:33]
	s_add_u32 s4, s4, s0
	s_addc_u32 s5, s5, 0
	v_lshl_add_u64 v[26:27], s[4:5], 0, v[30:31]
	v_lshl_add_u64 v[28:29], s[4:5], 0, v[32:33]
	s_add_u32 s4, s4, s0
	s_addc_u32 s5, s5, 0
	s_cmp_eq_u64 s[8:9], 0
	v_lshl_add_u64 v[30:31], s[4:5], 0, v[30:31]
	v_lshl_add_u64 v[32:33], s[4:5], 0, v[32:33]
	s_cselect_b64 s[4:5], -1, 0
	s_and_b64 s[14:15], s[4:5], exec
	s_cselect_b32 s0, s13, s9
	s_cselect_b32 s8, s12, s8
	s_ashr_i32 s11, s10, 31
	v_mov_b32_e32 v152, s8
	v_mov_b32_e32 v153, s0
	v_lshl_add_u64 v[154:155], s[10:11], 0, v[130:131]
	v_readlane_b32 s12, v156, 4
	v_readlane_b32 s11, v156, 5
	v_lshl_add_u64 v[152:153], v[154:155], 2, v[152:153]
	s_waitcnt vmcnt(6)
	v_mul_f32_e32 v114, s12, v114
	v_mul_f32_e32 v118, s11, v118
	global_load_dwordx4 v[42:45], v[10:11], off nt
	s_nop 0
	global_load_dwordx4 v[10:13], v[12:13], off nt
	s_nop 0
	global_load_dwordx4 v[50:53], v[18:19], off nt
	s_nop 0
	global_load_dwordx4 v[18:21], v[20:21], off nt
	s_nop 0
	global_load_dwordx4 v[54:57], v[22:23], off nt
	s_nop 0
	global_load_dwordx4 v[22:25], v[24:25], off nt
	s_nop 0
	global_load_dwordx4 v[62:65], v[26:27], off nt
	s_nop 0
	global_load_dwordx4 v[26:29], v[28:29], off nt
	s_nop 0
	global_load_dwordx4 v[58:61], v[30:31], off nt
	s_nop 0
	global_load_dwordx4 v[30:33], v[32:33], off nt
	v_med3_f32 v114, v114, s25, v151
	v_med3_f32 v118, v118, s25, v151
	v_mov_b32_e32 v153, 0
	v_cvt_pk_fp8_f32 v153, v114, v118
	v_readlane_b32 s14, v156, 6
	v_readlane_b32 s13, v156, 7
	v_readlane_b32 s9, v156, 0
	v_readlane_b32 s8, v156, 1
	v_mul_f32_e32 v126, s14, v126
	v_mul_f32_e32 v118, s13, v122
	v_med3_f32 v114, v126, s25, v151
	v_med3_f32 v118, v118, s25, v151
	v_mul_f32_e32 v98, s9, v98
	v_mul_f32_e32 v102, s8, v102
	v_cvt_pk_fp8_f32 v153, v114, v118 op_sel:[0,0,1]
	v_med3_f32 v98, v98, s25, v151
	v_med3_f32 v102, v102, s25, v151
	v_mov_b32_e32 v114, 0
	v_cvt_pk_fp8_f32 v114, v98, v102
	v_readlane_b32 s10, v156, 2
	v_readlane_b32 s0, v156, 3
	v_mul_f32_e32 v99, s9, v99
	v_mul_f32_e32 v110, s10, v110
	v_mul_f32_e32 v102, s0, v106
	v_med3_f32 v98, v110, s25, v151
	v_med3_f32 v102, v102, s25, v151
	v_cvt_pk_fp8_f32 v114, v98, v102 op_sel:[0,0,1]
	v_mul_f32_e32 v102, s12, v115
	v_mul_f32_e32 v106, s11, v119
	v_med3_f32 v102, v102, s25, v151
	v_med3_f32 v106, v106, s25, v151
	v_mov_b32_e32 v110, 0
	v_cvt_pk_fp8_f32 v110, v102, v106
	v_mul_f32_e32 v98, s14, v127
	v_mul_f32_e32 v102, s13, v123
	v_med3_f32 v98, v98, s25, v151
	v_med3_f32 v102, v102, s25, v151
	v_cvt_pk_fp8_f32 v110, v98, v102 op_sel:[0,0,1]
	v_mul_f32_e32 v102, s8, v103
	v_med3_f32 v99, v99, s25, v151
	v_med3_f32 v102, v102, s25, v151
	v_mov_b32_e32 v103, 0
	v_cvt_pk_fp8_f32 v103, v99, v102
	v_mul_f32_e32 v98, s10, v111
	v_mul_f32_e32 v99, s0, v107
	v_med3_f32 v98, v98, s25, v151
	v_med3_f32 v99, v99, s25, v151
	v_cvt_pk_fp8_f32 v103, v98, v99 op_sel:[0,0,1]
	v_mul_f32_e32 v99, s12, v116
	v_mul_f32_e32 v102, s11, v120
	v_med3_f32 v99, v99, s25, v151
	v_med3_f32 v102, v102, s25, v151
	v_mov_b32_e32 v106, 0
	v_cvt_pk_fp8_f32 v106, v99, v102
	v_mul_f32_e32 v100, s9, v100
	v_mul_f32_e32 v102, s8, v104
	v_mul_f32_e32 v98, s14, v128
	v_mul_f32_e32 v99, s13, v124
	v_med3_f32 v100, v100, s25, v151
	v_med3_f32 v102, v102, s25, v151
	v_mov_b32_e32 v104, 0
	v_med3_f32 v98, v98, s25, v151
	v_med3_f32 v99, v99, s25, v151
	v_cvt_pk_fp8_f32 v104, v100, v102
	v_mul_f32_e32 v102, s12, v117
	v_mul_f32_e32 v107, s11, v121
	v_cvt_pk_fp8_f32 v106, v98, v99 op_sel:[0,0,1]
	v_mul_f32_e32 v99, s0, v108
	v_med3_f32 v102, v102, s25, v151
	v_med3_f32 v107, v107, s25, v151
	v_mov_b32_e32 v108, 0
	v_cvt_pk_fp8_f32 v108, v102, v107
	v_mul_f32_e32 v100, s14, v129
	v_mul_f32_e32 v102, s13, v125
	v_med3_f32 v100, v100, s25, v151
	v_med3_f32 v102, v102, s25, v151
; #define LAS __attribute__((address_space(3)))
; __device__ __forceinline__ void cvt8_pack(f32x4 (&v)[16], float gv, LAS unsigned char* lds, int sub, int wave, int lane) {
;     float gs[8];
; #pragma unroll
;     for (int i = 0; i < 8; ++i) gs[i] = __builtin_bit_cast(float, __builtin_amdgcn_readlane(__builtin_bit_cast(int, gv), i));
; #pragma unroll
;     for (int hf = 0; hf < 2; ++hf) { u32x4 w[2];
; #pragma unroll
;         for (int j = 0; j < 4; ++j) { const unsigned lo = pk4_fp8(v[0 + hf][j] * gs[0], v[2 + hf][j] * gs[1], v[4 + hf][j] * gs[2], v[6 + hf][j] * gs[3]), hi = pk4_fp8(v[8 + hf][j] * gs[4], v[10 + hf][j] * gs[5], v[12 + hf][j] * gs[6], v[14 + hf][j] * gs[7]);
;             if (j & 1) { w[j >> 1].z = lo; w[j >> 1].w = hi; } else { w[j >> 1].x = lo; w[j >> 1].y = hi; } }
;         const int sw = 8 * sub + 2 * (wave >> 1);
;         LAS unsigned char* p = lds + sub * 32768 + wave * 4096 + ((hf * 256 + 4 * lane) ^ (sw & 28)) * 8;
;         { const int o0 = 8 * (sw & 2), o1 = 16 - o0; const bool q = (lane >> 2) & 1;
;           *(LAS u32x4*)(p + (q ? o1 : o0)) = q ? w[1] : w[0]; *(LAS u32x4*)(p + (q ? o0 : o1)) = q ? w[0] : w[1]; } }
; }
; __device__ __forceinline__ void cvt8_phase(const Frame& F, const KArgs& a, const int bit, const int nb, const int s_lo, const int s_hi) {
;     ...
;     auto decode = [&](int s, int j) -> Cvt8Desc {
;         Cvt8Desc D;
;         if (s < S_WGU) { const int e = s / 64, rr = s % 64, kb4 = rr / 8, cb = rr % 8, kb = kb4 * 4 + j;
;             const int da = 4 * lane, db = 256 + 4 * lane;
;             D.W = a.in[20] + (size_t)e * DM * 2 * DFF; D.g = a.in[17]; D.ldw = 2 * DFF; D.k0 = kb * 64;
;             D.col0a = ((da & 255) < 128 ? 0 : DFF) + (cb * 2 + (da >> 8)) * 128 + (da & 127); D.col0b = ((db & 255) < 128 ? 0 : DFF) + (cb * 2 + (db >> 8)) * 128 + (db & 127);
;             D.dst = ws + WS_WGU + ((size_t)e * 2 * DFF + cb * 512) * DM + kb4 * 256; return D; }
;         s -= S_WGU;
;         { const int e = s / 32, rr = s % 32, kb4 = rr / 4, cb = rr % 4, kb = kb4 * 4 + j;
;             D.W = a.in[22] + (size_t)e * DFF * DM; D.g = nullptr; D.ldw = DM; D.k0 = kb * 64; D.col0a = cb * 512 + 4 * lane; D.col0b = cb * 512 + 256 + 4 * lane;
;             D.dst = ws + WS_WD + ((size_t)e * DM + cb * 512) * DFF + kb4 * 256; return D; }
;     };
	v_cvt_pk_fp8_f32 v108, v100, v102 op_sel:[0,0,1]
	v_mul_f32_e32 v101, s9, v101
	v_mul_f32_e32 v102, s8, v105
	v_med3_f32 v101, v101, s25, v151
	v_med3_f32 v102, v102, s25, v151
	v_mov_b32_e32 v105, 0
	v_cvt_pk_fp8_f32 v105, v101, v102
	v_mul_f32_e32 v98, s10, v112
	v_mul_f32_e32 v100, s10, v113
	v_mul_f32_e32 v101, s0, v109
	v_med3_f32 v98, v98, s25, v151
	v_med3_f32 v100, v100, s25, v151
	v_med3_f32 v101, v101, s25, v151
	v_med3_f32 v99, v99, s25, v151
	v_cvt_pk_fp8_f32 v105, v100, v101 op_sel:[0,0,1]
	v_cvt_pk_fp8_f32 v104, v98, v99 op_sel:[0,0,1]
	v_cndmask_b32_e64 v101, v108, v110, s[2:3]
	v_cndmask_b32_e64 v99, v106, v153, s[2:3]
	v_cndmask_b32_e64 v100, v105, v103, s[2:3]
	v_cndmask_b32_e64 v98, v104, v114, s[2:3]
	v_add_u32_e32 v102, v143, v137
	ds_write_b128 v102, v[98:101] offset:32768
	v_cndmask_b32_e64 v101, v110, v108, s[2:3]
	v_cndmask_b32_e64 v100, v103, v105, s[2:3]
	v_cndmask_b32_e64 v99, v153, v106, s[2:3]
	v_cndmask_b32_e64 v98, v114, v104, s[2:3]
	v_add_u32_e32 v102, v143, v138
	v_mul_f32_e32 v85, s12, v85
	v_mul_f32_e32 v89, s11, v89
	ds_write_b128 v102, v[98:101] offset:32768
	v_med3_f32 v85, v85, s25, v151
	v_med3_f32 v89, v89, s25, v151
	v_mov_b32_e32 v98, 0
	v_cvt_pk_fp8_f32 v98, v85, v89
	v_mul_f32_e32 v93, s14, v93
	v_mul_f32_e32 v89, s13, v97
	v_med3_f32 v85, v93, s25, v151
	v_med3_f32 v89, v89, s25, v151
	v_mul_f32_e32 v66, s9, v66
	v_mul_f32_e32 v70, s8, v70
	v_cvt_pk_fp8_f32 v98, v85, v89 op_sel:[0,0,1]
	v_med3_f32 v66, v66, s25, v151
	v_med3_f32 v70, v70, s25, v151
	v_mov_b32_e32 v85, 0
	v_cvt_pk_fp8_f32 v85, v66, v70
	v_mul_f32_e32 v78, s10, v78
	v_mul_f32_e32 v70, s0, v74
	v_med3_f32 v66, v78, s25, v151
	v_med3_f32 v70, v70, s25, v151
	v_cvt_pk_fp8_f32 v85, v66, v70 op_sel:[0,0,1]
	v_mul_f32_e32 v70, s12, v82
	v_mul_f32_e32 v74, s11, v86
	v_med3_f32 v70, v70, s25, v151
	v_med3_f32 v74, v74, s25, v151
	v_mov_b32_e32 v78, 0
	v_cvt_pk_fp8_f32 v78, v70, v74
	v_mul_f32_e32 v66, s14, v90
	v_mul_f32_e32 v70, s13, v94
	v_med3_f32 v66, v66, s25, v151
	v_med3_f32 v70, v70, s25, v151
	v_cvt_pk_fp8_f32 v78, v66, v70 op_sel:[0,0,1]
	v_mul_f32_e32 v67, s9, v67
	v_mul_f32_e32 v70, s8, v71
	v_med3_f32 v67, v67, s25, v151
	v_med3_f32 v70, v70, s25, v151
	v_mov_b32_e32 v71, 0
	v_cvt_pk_fp8_f32 v71, v67, v70
	v_mul_f32_e32 v66, s10, v79
	v_mul_f32_e32 v67, s0, v75
	v_med3_f32 v66, v66, s25, v151
	v_med3_f32 v67, v67, s25, v151
	v_cvt_pk_fp8_f32 v71, v66, v67 op_sel:[0,0,1]
	v_mul_f32_e32 v67, s12, v83
	v_mul_f32_e32 v70, s11, v87
	v_med3_f32 v67, v67, s25, v151
	v_med3_f32 v70, v70, s25, v151
	v_mov_b32_e32 v74, 0
	v_cvt_pk_fp8_f32 v74, v67, v70
	v_mul_f32_e32 v66, s14, v91
	v_mul_f32_e32 v67, s13, v95
	v_med3_f32 v66, v66, s25, v151
	v_med3_f32 v67, v67, s25, v151
	v_cvt_pk_fp8_f32 v74, v66, v67 op_sel:[0,0,1]
	v_mul_f32_e32 v67, s0, v76
	v_mul_f32_e32 v75, s12, v84
	v_mul_f32_e32 v76, s11, v88
	v_mul_f32_e32 v68, s9, v68
	v_mul_f32_e32 v70, s8, v72
	v_med3_f32 v75, v75, s25, v151
	v_med3_f32 v76, v76, s25, v151
	v_mov_b32_e32 v79, 0
	v_mul_f32_e32 v69, s9, v69
	v_mul_f32_e32 v73, s8, v73
	v_med3_f32 v68, v68, s25, v151
	v_med3_f32 v70, v70, s25, v151
	v_mov_b32_e32 v72, 0
	v_cvt_pk_fp8_f32 v79, v75, v76
	v_med3_f32 v69, v69, s25, v151
	v_med3_f32 v73, v73, s25, v151
	v_mov_b32_e32 v76, 0
	v_cvt_pk_fp8_f32 v72, v68, v70
	v_cvt_pk_fp8_f32 v76, v69, v73
	v_mul_f32_e32 v66, s10, v80
	v_mul_f32_e32 v68, s14, v92
	v_mul_f32_e32 v70, s13, v96
	v_mul_f32_e32 v75, s10, v81
	v_mul_f32_e32 v73, s0, v77
	v_med3_f32 v66, v66, s25, v151
	v_med3_f32 v67, v67, s25, v151
	v_med3_f32 v68, v68, s25, v151
	v_med3_f32 v70, v70, s25, v151
	v_med3_f32 v69, v75, s25, v151
	v_med3_f32 v73, v73, s25, v151
	v_cvt_pk_fp8_f32 v76, v69, v73 op_sel:[0,0,1]
	v_cvt_pk_fp8_f32 v79, v68, v70 op_sel:[0,0,1]
	v_cvt_pk_fp8_f32 v72, v66, v67 op_sel:[0,0,1]
	v_cndmask_b32_e64 v69, v98, v74, s[2:3]
	v_cndmask_b32_e64 v68, v76, v71, s[2:3]
	v_cndmask_b32_e64 v67, v79, v78, s[2:3]
	v_cndmask_b32_e64 v66, v72, v85, s[2:3]
	v_add_u32_e32 v70, v144, v137
	ds_write_b128 v70, v[66:69] offset:32768
	v_cndmask_b32_e64 v69, v74, v98, s[2:3]
	v_cndmask_b32_e64 v68, v71, v76, s[2:3]
	v_cndmask_b32_e64 v67, v78, v79, s[2:3]
	v_cndmask_b32_e64 v66, v85, v72, s[2:3]
	v_add_u32_e32 v70, v144, v138
	s_and_b64 vcc, exec, s[6:7]
	v_readfirstlane_b32 s10, v0
	ds_write_b128 v70, v[66:69] offset:32768
	s_cbranch_vccz .LBB0_1129
	s_add_i32 s0, s19, 0xfffff800
	s_lshr_b32 s0, s0, 5
	v_readlane_b32 s36, v252, 22
	s_lshl_b64 s[8:9], s[0:1], 24
	v_readlane_b32 s48, v252, 34
	v_readlane_b32 s49, v252, 35
	s_add_u32 s14, s48, s8
	s_addc_u32 s15, s49, s9
	s_lshl_b32 s0, s19, 6
	s_and_b32 s10, s0, 0x700
	s_lshl_b32 s0, s19, 9
	s_and_b32 s0, s0, 0x600
	v_readlane_b32 s37, v252, 23
	v_readlane_b32 s38, v252, 24
	v_readlane_b32 s39, v252, 25
	v_readlane_b32 s40, v252, 26
	v_readlane_b32 s41, v252, 27
	v_readlane_b32 s42, v252, 28
	v_readlane_b32 s43, v252, 29
	v_readlane_b32 s44, v252, 30
	v_readlane_b32 s45, v252, 31
	v_readlane_b32 s46, v252, 32
	v_readlane_b32 s47, v252, 33
	v_readlane_b32 s50, v252, 36
	v_readlane_b32 s51, v252, 37
	v_or_b32_e32 v68, s0, v1
	v_or_b32_e32 v66, s0, v135
	s_mov_b64 s[12:13], 0
	s_mov_b64 s[16:17], 0x800
	s_cbranch_execz .LBB0_1130
	s_branch .LBB0_1131

; __device__ __forceinline__ void cvt8_load(const Cvt8Desc& d, f32x4 (&v)[16], float& gv, int wave, int lane) {
;     const float* rowp = d.W + (size_t)(d.k0 + 8 * wave) * d.ldw;
; #pragma unroll
;     for (int i = 0; i < 8; ++i) { v[2 * i] = __builtin_nontemporal_load((const f32x4*)(rowp + d.col0a)); v[2 * i + 1] = __builtin_nontemporal_load((const f32x4*)(rowp + d.col0b)); rowp += d.ldw; }
;     const float* gp = d.g ? d.g : d.W; const float gl = gp[d.k0 + 8 * wave + (lane & 7)]; gv = d.g ? gl * W8_SCALE : W8_SCALE;
; }
; __device__ __forceinline__ void cvt8_pack(f32x4 (&v)[16], float gv, LAS unsigned char* lds, int sub, int wave, int lane) {
;     float gs[8];
; #pragma unroll
;     for (int i = 0; i < 8; ++i) gs[i] = __builtin_bit_cast(float, __builtin_amdgcn_readlane(__builtin_bit_cast(int, gv), i));
; #pragma unroll
;     for (int hf = 0; hf < 2; ++hf) { u32x4 w[2];
; #pragma unroll
;         for (int j = 0; j < 4; ++j) { const unsigned lo = pk4_fp8(v[0 + hf][j] * gs[0], v[2 + hf][j] * gs[1], v[4 + hf][j] * gs[2], v[6 + hf][j] * gs[3]), hi = pk4_fp8(v[8 + hf][j] * gs[4], v[10 + hf][j] * gs[5], v[12 + hf][j] * gs[6], v[14 + hf][j] * gs[7]);
;             if (j & 1) { w[j >> 1].z = lo; w[j >> 1].w = hi; } else { w[j >> 1].x = lo; w[j >> 1].y = hi; } }
;         const int sw = 8 * sub + 2 * (wave >> 1);
;         LAS unsigned char* p = lds + sub * 32768 + wave * 4096 + ((hf * 256 + 4 * lane) ^ (sw & 28)) * 8;
;         { const int o0 = 8 * (sw & 2), o1 = 16 - o0; const bool q = (lane >> 2) & 1;
;           *(LAS u32x4*)(p + (q ? o1 : o0)) = q ? w[1] : w[0]; *(LAS u32x4*)(p + (q ? o0 : o1)) = q ? w[0] : w[1]; } }
; }
; __device__ __forceinline__ void cvt8_phase(const Frame& F, const KArgs& a, const int bit, const int nb, const int s_lo, const int s_hi) {
;     ...
;     while (sidx < s_hi) {
;         const int snext = sidx + nb; const bool more = snext < s_hi;
;         { Cvt8Desc d1 = decode(sidx, 1); cvt8_load(d1, vb, gb, wave, lane); } cvt8_pack(va, ga, F.lds, 0, wave, lane);
;         { Cvt8Desc d2 = decode(sidx, 2); cvt8_load(d2, va, ga, wave, lane); } cvt8_pack(vb, gb, F.lds, 1, wave, lane);
;         { Cvt8Desc d3 = decode(sidx, 3); cvt8_load(d3, vb, gb, wave, lane); } cvt8_pack(va, ga, F.lds, 2, wave, lane);
;         { Cvt8Desc dn = decode(more ? snext : sidx, 0); cvt8_load(dn, va, ga, wave, lane); } cvt8_pack(vb, gb, F.lds, 3, wave, lane);
.LBB0_1131:
	s_add_i32 s17, s19, 0x70
	s_cmpk_gt_i32 s19, 0xb8f
	s_cselect_b64 s[8:9], -1, 0
	s_add_i32 s0, s18, s10
	v_mul_f32_e32 v67, 0x42800000, v159
	s_addk_i32 s0, 0xc0
	v_cndmask_b32_e64 v156, v67, v134, s[4:5]
	s_mul_hi_i32 s5, s16, s0
	s_mul_i32 s4, s16, s0
	s_lshl_b64 s[4:5], s[4:5], 2
	s_add_u32 s28, s14, s4
	s_addc_u32 s29, s15, s5
	s_lshl_b32 s0, s16, 2
	s_add_u32 s30, s28, s0
	s_addc_u32 s31, s29, 0
	s_add_u32 s34, s30, s0
	s_addc_u32 s35, s31, 0
	s_add_u32 s36, s34, s0
	s_addc_u32 s37, s35, 0
	s_add_u32 s38, s36, s0
	s_addc_u32 s39, s37, 0
	s_add_u32 s40, s38, s0
	s_addc_u32 s41, s39, 0
	s_add_u32 s42, s40, s0
	s_addc_u32 s43, s41, 0
	s_add_u32 s44, s42, s0
	s_addc_u32 s45, s43, 0
	s_cmp_eq_u64 s[12:13], 0
	s_cselect_b64 s[4:5], -1, 0
	s_and_b64 s[46:47], s[4:5], exec
	v_ashrrev_i32_e32 v69, 31, v68
	v_ashrrev_i32_e32 v67, 31, v66
	s_cselect_b32 s0, s14, s12
	s_cselect_b32 s12, s15, s13
	s_ashr_i32 s11, s10, 31
	v_lshlrev_b64 v[94:95], 2, v[68:69]
	v_lshlrev_b64 v[96:97], 2, v[66:67]
	v_lshl_add_u64 v[68:69], s[28:29], 0, v[94:95]
	v_lshl_add_u64 v[66:67], s[28:29], 0, v[96:97]
	v_lshl_add_u64 v[70:71], s[30:31], 0, v[94:95]
	v_lshl_add_u64 v[72:73], s[30:31], 0, v[96:97]
	v_lshl_add_u64 v[74:75], s[34:35], 0, v[94:95]
	v_lshl_add_u64 v[76:77], s[34:35], 0, v[96:97]
	v_mov_b32_e32 v152, s0
	v_mov_b32_e32 v153, s12
	v_lshl_add_u64 v[154:155], s[10:11], 0, v[130:131]
	v_readlane_b32 s14, v156, 4
	v_readlane_b32 s13, v156, 5
	global_load_dwordx4 v[98:101], v[68:69], off nt
	s_nop 0
	global_load_dwordx4 v[66:69], v[66:67], off nt
	s_nop 0
	global_load_dwordx4 v[102:105], v[70:71], off nt
	s_nop 0
	global_load_dwordx4 v[70:73], v[72:73], off nt
	s_nop 0
	global_load_dwordx4 v[110:113], v[74:75], off nt
	global_load_dwordx4 v[78:81], v[76:77], off nt
	v_lshl_add_u64 v[74:75], s[36:37], 0, v[94:95]
	v_lshl_add_u64 v[76:77], s[36:37], 0, v[96:97]
	v_lshl_add_u64 v[82:83], s[38:39], 0, v[94:95]
	v_lshl_add_u64 v[84:85], s[38:39], 0, v[96:97]
	v_lshl_add_u64 v[86:87], s[40:41], 0, v[94:95]
	v_lshl_add_u64 v[88:89], s[40:41], 0, v[96:97]
	v_lshl_add_u64 v[90:91], s[42:43], 0, v[94:95]
	v_lshl_add_u64 v[92:93], s[42:43], 0, v[96:97]
	v_lshl_add_u64 v[94:95], s[44:45], 0, v[94:95]
	v_lshl_add_u64 v[96:97], s[44:45], 0, v[96:97]
	v_lshl_add_u64 v[152:153], v[154:155], 2, v[152:153]
	s_waitcnt vmcnt(6)
	v_mul_f32_e32 v50, s14, v50
	v_mul_f32_e32 v54, s13, v54
	global_load_dwordx4 v[106:109], v[74:75], off nt
	s_nop 0
	global_load_dwordx4 v[74:77], v[76:77], off nt
	s_nop 0
	global_load_dwordx4 v[114:117], v[82:83], off nt
	s_nop 0
	global_load_dwordx4 v[82:85], v[84:85], off nt
	s_nop 0
	global_load_dwordx4 v[118:121], v[86:87], off nt
	s_nop 0
	global_load_dwordx4 v[86:89], v[88:89], off nt
	s_nop 0
	global_load_dwordx4 v[126:129], v[90:91], off nt
	s_nop 0
	global_load_dwordx4 v[90:93], v[92:93], off nt
	s_nop 0
	global_load_dwordx4 v[122:125], v[94:95], off nt
	s_nop 0
	global_load_dwordx4 v[94:97], v[96:97], off nt
	v_med3_f32 v50, v50, s25, v151
	v_med3_f32 v54, v54, s25, v151
	v_mov_b32_e32 v153, 0
	v_cvt_pk_fp8_f32 v153, v50, v54
	v_readlane_b32 s16, v156, 6
	v_readlane_b32 s15, v156, 7
	v_readlane_b32 s11, v156, 0
	v_readlane_b32 s10, v156, 1
	v_mul_f32_e32 v62, s16, v62
	v_mul_f32_e32 v54, s15, v58
	v_med3_f32 v50, v62, s25, v151
	v_med3_f32 v54, v54, s25, v151
	v_mul_f32_e32 v34, s11, v34
	v_mul_f32_e32 v38, s10, v38
	v_cvt_pk_fp8_f32 v153, v50, v54 op_sel:[0,0,1]
	v_med3_f32 v34, v34, s25, v151
	v_med3_f32 v38, v38, s25, v151
	v_mov_b32_e32 v50, 0
	v_cvt_pk_fp8_f32 v50, v34, v38
	v_readlane_b32 s12, v156, 2
	v_readlane_b32 s0, v156, 3
	v_mul_f32_e32 v35, s11, v35
	v_mul_f32_e32 v46, s12, v46
	v_mul_f32_e32 v38, s0, v42
	v_med3_f32 v34, v46, s25, v151
	v_med3_f32 v38, v38, s25, v151
	v_cvt_pk_fp8_f32 v50, v34, v38 op_sel:[0,0,1]
	v_mul_f32_e32 v38, s14, v51
	v_mul_f32_e32 v42, s13, v55
	v_med3_f32 v38, v38, s25, v151
	v_med3_f32 v42, v42, s25, v151
	v_mov_b32_e32 v46, 0
	v_cvt_pk_fp8_f32 v46, v38, v42
	v_mul_f32_e32 v34, s16, v63
	v_mul_f32_e32 v38, s15, v59
	v_med3_f32 v34, v34, s25, v151
	v_med3_f32 v38, v38, s25, v151
	v_cvt_pk_fp8_f32 v46, v34, v38 op_sel:[0,0,1]
	v_mul_f32_e32 v38, s10, v39
	v_med3_f32 v35, v35, s25, v151
	v_med3_f32 v38, v38, s25, v151
	v_mov_b32_e32 v39, 0
	v_cvt_pk_fp8_f32 v39, v35, v38
	v_mul_f32_e32 v34, s12, v47
	v_mul_f32_e32 v35, s0, v43
	v_med3_f32 v34, v34, s25, v151
	v_med3_f32 v35, v35, s25, v151
	v_cvt_pk_fp8_f32 v39, v34, v35 op_sel:[0,0,1]
	v_mul_f32_e32 v35, s14, v52
	v_mul_f32_e32 v38, s13, v56
	v_med3_f32 v35, v35, s25, v151
	v_med3_f32 v38, v38, s25, v151
	v_mov_b32_e32 v42, 0
	v_cvt_pk_fp8_f32 v42, v35, v38
	v_mul_f32_e32 v36, s11, v36
	v_mul_f32_e32 v38, s10, v40
	v_mul_f32_e32 v34, s16, v64
	v_mul_f32_e32 v35, s15, v60
	v_med3_f32 v36, v36, s25, v151
	v_med3_f32 v38, v38, s25, v151
	v_mov_b32_e32 v40, 0
	v_med3_f32 v34, v34, s25, v151
	v_med3_f32 v35, v35, s25, v151
	v_cvt_pk_fp8_f32 v40, v36, v38
	v_mul_f32_e32 v38, s14, v53
	v_mul_f32_e32 v43, s13, v57
	v_cvt_pk_fp8_f32 v42, v34, v35 op_sel:[0,0,1]
	v_mul_f32_e32 v35, s0, v44
	v_med3_f32 v38, v38, s25, v151
	v_med3_f32 v43, v43, s25, v151
	v_mov_b32_e32 v44, 0
	v_cvt_pk_fp8_f32 v44, v38, v43
; #define LAS __attribute__((address_space(3)))
; __device__ __forceinline__ void cvt8_pack(f32x4 (&v)[16], float gv, LAS unsigned char* lds, int sub, int wave, int lane) {
;     float gs[8];
; #pragma unroll
;     for (int i = 0; i < 8; ++i) gs[i] = __builtin_bit_cast(float, __builtin_amdgcn_readlane(__builtin_bit_cast(int, gv), i));
; #pragma unroll
;     for (int hf = 0; hf < 2; ++hf) { u32x4 w[2];
; #pragma unroll
;         for (int j = 0; j < 4; ++j) { const unsigned lo = pk4_fp8(v[0 + hf][j] * gs[0], v[2 + hf][j] * gs[1], v[4 + hf][j] * gs[2], v[6 + hf][j] * gs[3]), hi = pk4_fp8(v[8 + hf][j] * gs[4], v[10 + hf][j] * gs[5], v[12 + hf][j] * gs[6], v[14 + hf][j] * gs[7]);
;             if (j & 1) { w[j >> 1].z = lo; w[j >> 1].w = hi; } else { w[j >> 1].x = lo; w[j >> 1].y = hi; } }
;         const int sw = 8 * sub + 2 * (wave >> 1);
;         LAS unsigned char* p = lds + sub * 32768 + wave * 4096 + ((hf * 256 + 4 * lane) ^ (sw & 28)) * 8;
;         { const int o0 = 8 * (sw & 2), o1 = 16 - o0; const bool q = (lane >> 2) & 1;
;           *(LAS u32x4*)(p + (q ? o1 : o0)) = q ? w[1] : w[0]; *(LAS u32x4*)(p + (q ? o0 : o1)) = q ? w[0] : w[1]; } }
; }
; __device__ __forceinline__ void cvt8_phase(const Frame& F, const KArgs& a, const int bit, const int nb, const int s_lo, const int s_hi) {
;     ...
;     auto decode = [&](int s, int j) -> Cvt8Desc {
;         Cvt8Desc D;
;         if (s < S_WGU) { const int e = s / 64, rr = s % 64, kb4 = rr / 8, cb = rr % 8, kb = kb4 * 4 + j;
;             const int da = 4 * lane, db = 256 + 4 * lane;
;             D.W = a.in[20] + (size_t)e * DM * 2 * DFF; D.g = a.in[17]; D.ldw = 2 * DFF; D.k0 = kb * 64;
;             D.col0a = ((da & 255) < 128 ? 0 : DFF) + (cb * 2 + (da >> 8)) * 128 + (da & 127); D.col0b = ((db & 255) < 128 ? 0 : DFF) + (cb * 2 + (db >> 8)) * 128 + (db & 127);
;             D.dst = ws + WS_WGU + ((size_t)e * 2 * DFF + cb * 512) * DM + kb4 * 256; return D; }
;         s -= S_WGU;
;         { const int e = s / 32, rr = s % 32, kb4 = rr / 4, cb = rr % 4, kb = kb4 * 4 + j;
;             D.W = a.in[22] + (size_t)e * DFF * DM; D.g = nullptr; D.ldw = DM; D.k0 = kb * 64; D.col0a = cb * 512 + 4 * lane; D.col0b = cb * 512 + 256 + 4 * lane;
;             D.dst = ws + WS_WD + ((size_t)e * DM + cb * 512) * DFF + kb4 * 256; return D; }
;     };
;     f32x4 va[16], vb[16]; float ga = 1.f, gb = 1.f;
;     int sidx = s_lo + bit;
	v_mul_f32_e32 v36, s16, v65
	v_mul_f32_e32 v38, s15, v61
	v_med3_f32 v36, v36, s25, v151
	v_med3_f32 v38, v38, s25, v151
	v_cvt_pk_fp8_f32 v44, v36, v38 op_sel:[0,0,1]
	v_mul_f32_e32 v37, s11, v37
	v_mul_f32_e32 v38, s10, v41
	v_med3_f32 v37, v37, s25, v151
	v_med3_f32 v38, v38, s25, v151
	v_mov_b32_e32 v41, 0
	v_cvt_pk_fp8_f32 v41, v37, v38
	v_mul_f32_e32 v34, s12, v48
	v_mul_f32_e32 v36, s12, v49
	v_mul_f32_e32 v37, s0, v45
	v_med3_f32 v34, v34, s25, v151
	v_med3_f32 v36, v36, s25, v151
	v_med3_f32 v37, v37, s25, v151
	v_med3_f32 v35, v35, s25, v151
	v_cvt_pk_fp8_f32 v41, v36, v37 op_sel:[0,0,1]
	v_cvt_pk_fp8_f32 v40, v34, v35 op_sel:[0,0,1]
	v_cndmask_b32_e64 v37, v44, v46, s[2:3]
	v_cndmask_b32_e64 v35, v42, v153, s[2:3]
	v_cndmask_b32_e64 v36, v41, v39, s[2:3]
	v_cndmask_b32_e64 v34, v40, v50, s[2:3]
	v_add_u32_e32 v38, v145, v137
	ds_write_b128 v38, v[34:37]
	v_cndmask_b32_e64 v37, v46, v44, s[2:3]
	v_cndmask_b32_e64 v36, v39, v41, s[2:3]
	v_cndmask_b32_e64 v35, v153, v42, s[2:3]
	v_cndmask_b32_e64 v34, v50, v40, s[2:3]
	v_add_u32_e32 v38, v145, v138
	v_mul_f32_e32 v21, s14, v21
	v_mul_f32_e32 v25, s13, v25
	ds_write_b128 v38, v[34:37]
	v_med3_f32 v21, v21, s25, v151
	v_med3_f32 v25, v25, s25, v151
	v_mov_b32_e32 v34, 0
	v_cvt_pk_fp8_f32 v34, v21, v25
	v_mul_f32_e32 v29, s16, v29
	v_mul_f32_e32 v25, s15, v33
	v_med3_f32 v21, v29, s25, v151
	v_med3_f32 v25, v25, s25, v151
	v_mul_f32_e32 v2, s11, v2
	v_mul_f32_e32 v6, s10, v6
	v_cvt_pk_fp8_f32 v34, v21, v25 op_sel:[0,0,1]
	v_med3_f32 v2, v2, s25, v151
	v_med3_f32 v6, v6, s25, v151
	v_mov_b32_e32 v21, 0
	v_cvt_pk_fp8_f32 v21, v2, v6
	v_mul_f32_e32 v14, s12, v14
	v_mul_f32_e32 v6, s0, v10
	v_med3_f32 v2, v14, s25, v151
	v_med3_f32 v6, v6, s25, v151
	v_cvt_pk_fp8_f32 v21, v2, v6 op_sel:[0,0,1]
	v_mul_f32_e32 v6, s14, v18
	v_mul_f32_e32 v10, s13, v22
	v_med3_f32 v6, v6, s25, v151
	v_med3_f32 v10, v10, s25, v151
	v_mov_b32_e32 v14, 0
	v_cvt_pk_fp8_f32 v14, v6, v10
	v_mul_f32_e32 v2, s16, v26
	v_mul_f32_e32 v6, s15, v30
	v_med3_f32 v2, v2, s25, v151
	v_med3_f32 v6, v6, s25, v151
	v_cvt_pk_fp8_f32 v14, v2, v6 op_sel:[0,0,1]
	v_mul_f32_e32 v3, s11, v3
	v_mul_f32_e32 v6, s10, v7
	v_med3_f32 v3, v3, s25, v151
	v_med3_f32 v6, v6, s25, v151
	v_mov_b32_e32 v7, 0
	v_cvt_pk_fp8_f32 v7, v3, v6
	v_mul_f32_e32 v2, s12, v15
	v_mul_f32_e32 v3, s0, v11
	v_med3_f32 v2, v2, s25, v151
	v_med3_f32 v3, v3, s25, v151
	v_cvt_pk_fp8_f32 v7, v2, v3 op_sel:[0,0,1]
	v_mul_f32_e32 v3, s14, v19
	v_mul_f32_e32 v6, s13, v23
	v_med3_f32 v3, v3, s25, v151
	v_med3_f32 v6, v6, s25, v151
	v_mov_b32_e32 v10, 0
	v_cvt_pk_fp8_f32 v10, v3, v6
	v_mul_f32_e32 v2, s16, v27
	v_mul_f32_e32 v3, s15, v31
	v_med3_f32 v2, v2, s25, v151
	v_med3_f32 v3, v3, s25, v151
	v_cvt_pk_fp8_f32 v10, v2, v3 op_sel:[0,0,1]
	v_mul_f32_e32 v3, s0, v12
	v_mul_f32_e32 v11, s14, v20
	v_mul_f32_e32 v12, s13, v24
	v_mul_f32_e32 v4, s11, v4
	v_mul_f32_e32 v6, s10, v8
	v_med3_f32 v11, v11, s25, v151
	v_med3_f32 v12, v12, s25, v151
	v_mov_b32_e32 v15, 0
	v_mul_f32_e32 v5, s11, v5
	v_mul_f32_e32 v9, s10, v9
	v_med3_f32 v4, v4, s25, v151
	v_med3_f32 v6, v6, s25, v151
	v_mov_b32_e32 v8, 0
	v_cvt_pk_fp8_f32 v15, v11, v12
	v_med3_f32 v5, v5, s25, v151
	v_med3_f32 v9, v9, s25, v151
	v_mov_b32_e32 v12, 0
	v_cvt_pk_fp8_f32 v8, v4, v6
	v_cvt_pk_fp8_f32 v12, v5, v9
	v_mul_f32_e32 v2, s12, v16
	v_mul_f32_e32 v4, s16, v28
	v_mul_f32_e32 v6, s15, v32
	v_mul_f32_e32 v11, s12, v17
	v_mul_f32_e32 v9, s0, v13
	v_med3_f32 v2, v2, s25, v151
	v_med3_f32 v3, v3, s25, v151
	v_med3_f32 v4, v4, s25, v151
	v_med3_f32 v6, v6, s25, v151
	v_med3_f32 v5, v11, s25, v151
	v_med3_f32 v9, v9, s25, v151
	v_cvt_pk_fp8_f32 v12, v5, v9 op_sel:[0,0,1]
	v_cvt_pk_fp8_f32 v15, v4, v6 op_sel:[0,0,1]
	v_cvt_pk_fp8_f32 v8, v2, v3 op_sel:[0,0,1]
	s_cmpk_lt_i32 s19, 0xb90
	v_cndmask_b32_e64 v5, v34, v10, s[2:3]
	v_cndmask_b32_e64 v4, v12, v7, s[2:3]
	v_cndmask_b32_e64 v3, v15, v14, s[2:3]
	v_cndmask_b32_e64 v2, v8, v21, s[2:3]
	v_add_u32_e32 v6, v146, v137
	s_cselect_b32 s16, s17, s19
	ds_write_b128 v6, v[2:5]
	v_cndmask_b32_e64 v5, v10, v34, s[2:3]
	v_cndmask_b32_e64 v4, v7, v12, s[2:3]
	v_cndmask_b32_e64 v3, v14, v15, s[2:3]
	v_cndmask_b32_e64 v2, v21, v8, s[2:3]
	v_add_u32_e32 v6, v146, v138
	s_cmpk_gt_i32 s16, 0x7ff
	v_readfirstlane_b32 s0, v0
	ds_write_b128 v6, v[2:5]
	s_cbranch_scc0 .LBB0_1133
	s_add_i32 s0, s16, 0xfffff800
	s_lshr_b32 s0, s0, 5
	v_readlane_b32 s36, v252, 22
	s_lshl_b64 s[10:11], s[0:1], 24
	v_readlane_b32 s48, v252, 34
	v_readlane_b32 s49, v252, 35
	s_add_u32 s12, s48, s10
	s_addc_u32 s13, s49, s11
	s_lshl_b32 s10, s16, 9
	s_lshl_b32 s0, s16, 6
	s_and_b32 s10, s10, 0x600
	v_readlane_b32 s37, v252, 23
	v_readlane_b32 s38, v252, 24
	v_readlane_b32 s39, v252, 25
	v_readlane_b32 s40, v252, 26
	v_readlane_b32 s41, v252, 27
	v_readlane_b32 s42, v252, 28
	v_readlane_b32 s43, v252, 29
	v_readlane_b32 s44, v252, 30
	v_readlane_b32 s45, v252, 31
	v_readlane_b32 s46, v252, 32
	v_readlane_b32 s47, v252, 33
	v_readlane_b32 s50, v252, 36
	v_readlane_b32 s51, v252, 37
	s_and_b32 s0, s0, 0x700
	v_or_b32_e32 v4, s10, v1
	v_or_b32_e32 v2, s10, v135
	s_mov_b64 s[10:11], 0
	s_mov_b64 s[14:15], 0x800
	s_cbranch_execz .LBB0_1134
	s_branch .LBB0_1135

; __device__ __forceinline__ void cvt8_load(const Cvt8Desc& d, f32x4 (&v)[16], float& gv, int wave, int lane) {
;     const float* rowp = d.W + (size_t)(d.k0 + 8 * wave) * d.ldw;
; #pragma unroll
;     for (int i = 0; i < 8; ++i) { v[2 * i] = __builtin_nontemporal_load((const f32x4*)(rowp + d.col0a)); v[2 * i + 1] = __builtin_nontemporal_load((const f32x4*)(rowp + d.col0b)); rowp += d.ldw; }
;     const float* gp = d.g ? d.g : d.W; const float gl = gp[d.k0 + 8 * wave + (lane & 7)]; gv = d.g ? gl * W8_SCALE : W8_SCALE;
; }
; __device__ __forceinline__ void cvt8_pack(f32x4 (&v)[16], float gv, LAS unsigned char* lds, int sub, int wave, int lane) {
;     float gs[8];
; #pragma unroll
;     for (int i = 0; i < 8; ++i) gs[i] = __builtin_bit_cast(float, __builtin_amdgcn_readlane(__builtin_bit_cast(int, gv), i));
; #pragma unroll
;     for (int hf = 0; hf < 2; ++hf) { u32x4 w[2];
; #pragma unroll
;         for (int j = 0; j < 4; ++j) { const unsigned lo = pk4_fp8(v[0 + hf][j] * gs[0], v[2 + hf][j] * gs[1], v[4 + hf][j] * gs[2], v[6 + hf][j] * gs[3]), hi = pk4_fp8(v[8 + hf][j] * gs[4], v[10 + hf][j] * gs[5], v[12 + hf][j] * gs[6], v[14 + hf][j] * gs[7]);
;             if (j & 1) { w[j >> 1].z = lo; w[j >> 1].w = hi; } else { w[j >> 1].x = lo; w[j >> 1].y = hi; } }
;         const int sw = 8 * sub + 2 * (wave >> 1);
;         LAS unsigned char* p = lds + sub * 32768 + wave * 4096 + ((hf * 256 + 4 * lane) ^ (sw & 28)) * 8;
;         { const int o0 = 8 * (sw & 2), o1 = 16 - o0; const bool q = (lane >> 2) & 1;
;           *(LAS u32x4*)(p + (q ? o1 : o0)) = q ? w[1] : w[0]; *(LAS u32x4*)(p + (q ? o0 : o1)) = q ? w[0] : w[1]; } }
; }
; __device__ __forceinline__ void cvt8_phase(const Frame& F, const KArgs& a, const int bit, const int nb, const int s_lo, const int s_hi) {
;     ...
;     while (sidx < s_hi) {
;         const int snext = sidx + nb; const bool more = snext < s_hi;
;         { Cvt8Desc d1 = decode(sidx, 1); cvt8_load(d1, vb, gb, wave, lane); } cvt8_pack(va, ga, F.lds, 0, wave, lane);
;         { Cvt8Desc d2 = decode(sidx, 2); cvt8_load(d2, va, ga, wave, lane); } cvt8_pack(vb, gb, F.lds, 1, wave, lane);
;         { Cvt8Desc d3 = decode(sidx, 3); cvt8_load(d3, vb, gb, wave, lane); } cvt8_pack(va, ga, F.lds, 2, wave, lane);
;         { Cvt8Desc dn = decode(more ? snext : sidx, 0); cvt8_load(dn, va, ga, wave, lane); } cvt8_pack(vb, gb, F.lds, 3, wave, lane);
.LBB0_1135:
	v_mul_f32_e32 v3, 0x42800000, v160
	v_cndmask_b32_e64 v156, v3, v134, s[4:5]
	s_add_i32 s4, s0, s18
	s_mul_hi_i32 s5, s14, s4
	s_mul_i32 s4, s14, s4
	s_lshl_b64 s[4:5], s[4:5], 2
	s_add_u32 s4, s12, s4
	v_ashrrev_i32_e32 v5, 31, v4
	v_ashrrev_i32_e32 v3, 31, v2
	s_addc_u32 s5, s13, s5
	v_lshlrev_b64 v[30:31], 2, v[4:5]
	v_lshlrev_b64 v[32:33], 2, v[2:3]
	s_lshl_b32 s14, s14, 2
	v_lshl_add_u64 v[4:5], s[4:5], 0, v[30:31]
	v_lshl_add_u64 v[2:3], s[4:5], 0, v[32:33]
	s_add_u32 s4, s4, s14
	s_addc_u32 s5, s5, 0
	global_load_dwordx4 v[38:41], v[4:5], off nt
	global_load_dwordx4 v[6:9], v[2:3], off nt
	v_lshl_add_u64 v[2:3], s[4:5], 0, v[30:31]
	v_lshl_add_u64 v[4:5], s[4:5], 0, v[32:33]
	s_add_u32 s4, s4, s14
	s_addc_u32 s5, s5, 0
	global_load_dwordx4 v[42:45], v[2:3], off nt
	global_load_dwordx4 v[10:13], v[4:5], off nt
	v_lshl_add_u64 v[2:3], s[4:5], 0, v[30:31]
	v_lshl_add_u64 v[4:5], s[4:5], 0, v[32:33]
	s_add_u32 s4, s4, s14
	s_addc_u32 s5, s5, 0
	global_load_dwordx4 v[46:49], v[2:3], off nt
	global_load_dwordx4 v[14:17], v[4:5], off nt
	v_lshl_add_u64 v[2:3], s[4:5], 0, v[30:31]
	v_lshl_add_u64 v[4:5], s[4:5], 0, v[32:33]
	s_add_u32 s4, s4, s14
	s_addc_u32 s5, s5, 0
	v_lshl_add_u64 v[18:19], s[4:5], 0, v[30:31]
	v_lshl_add_u64 v[20:21], s[4:5], 0, v[32:33]
	s_add_u32 s4, s4, s14
	s_addc_u32 s5, s5, 0
	v_lshl_add_u64 v[22:23], s[4:5], 0, v[30:31]
	v_lshl_add_u64 v[24:25], s[4:5], 0, v[32:33]
	s_add_u32 s4, s4, s14
	s_addc_u32 s5, s5, 0
	v_lshl_add_u64 v[26:27], s[4:5], 0, v[30:31]
	v_lshl_add_u64 v[28:29], s[4:5], 0, v[32:33]
	s_add_u32 s4, s4, s14
	s_addc_u32 s5, s5, 0
	s_cmp_eq_u64 s[10:11], 0
	v_lshl_add_u64 v[30:31], s[4:5], 0, v[30:31]
	v_lshl_add_u64 v[32:33], s[4:5], 0, v[32:33]
	s_cselect_b64 s[4:5], -1, 0
	s_and_b64 s[14:15], s[4:5], exec
	s_cselect_b32 s11, s13, s11
	s_cselect_b32 s10, s12, s10
	v_add_u32_e32 v154, s0, v130
	v_mov_b32_e32 v152, s10
	v_mov_b32_e32 v153, s11
	v_ashrrev_i32_e32 v155, 31, v154
	v_readlane_b32 s14, v156, 4
	v_readlane_b32 s13, v156, 5
	v_lshl_add_u64 v[152:153], v[154:155], 2, v[152:153]
	s_waitcnt vmcnt(6)
	v_mul_f32_e32 v114, s14, v114
	v_mul_f32_e32 v118, s13, v118
	global_load_dwordx4 v[34:37], v[2:3], off nt
	s_nop 0
	global_load_dwordx4 v[2:5], v[4:5], off nt
	s_nop 0
	global_load_dwordx4 v[50:53], v[18:19], off nt
	s_nop 0
	global_load_dwordx4 v[18:21], v[20:21], off nt
	s_nop 0
	global_load_dwordx4 v[54:57], v[22:23], off nt
	s_nop 0
	global_load_dwordx4 v[22:25], v[24:25], off nt
	s_nop 0
	global_load_dwordx4 v[58:61], v[26:27], off nt
	s_nop 0
	global_load_dwordx4 v[26:29], v[28:29], off nt
	s_nop 0
	global_load_dwordx4 v[62:65], v[30:31], off nt
	s_nop 0
	global_load_dwordx4 v[30:33], v[32:33], off nt
	v_med3_f32 v114, v114, s25, v151
	global_load_dword v158, v[152:153], off offset:256
	global_load_dword v159, v[152:153], off offset:512
	global_load_dword v160, v[152:153], off offset:768
	global_load_dword v152, v[152:153], off
	v_med3_f32 v118, v118, s25, v151
	v_mov_b32_e32 v153, 0
	v_cvt_pk_fp8_f32 v153, v114, v118
	v_readlane_b32 s16, v156, 6
	v_readlane_b32 s15, v156, 7
	v_readlane_b32 s11, v156, 0
	v_readlane_b32 s10, v156, 1
	v_mul_f32_e32 v126, s16, v126
	v_mul_f32_e32 v118, s15, v122
	v_med3_f32 v114, v126, s25, v151
	v_med3_f32 v118, v118, s25, v151
	v_mul_f32_e32 v98, s11, v98
	v_mul_f32_e32 v102, s10, v102
	v_cvt_pk_fp8_f32 v153, v114, v118 op_sel:[0,0,1]
	v_med3_f32 v98, v98, s25, v151
	v_med3_f32 v102, v102, s25, v151
	v_mov_b32_e32 v114, 0
	v_cvt_pk_fp8_f32 v114, v98, v102
	v_readlane_b32 s12, v156, 2
	v_readlane_b32 s0, v156, 3
	v_mul_f32_e32 v99, s11, v99
	v_mul_f32_e32 v110, s12, v110
	v_mul_f32_e32 v102, s0, v106
	v_med3_f32 v98, v110, s25, v151
	v_med3_f32 v102, v102, s25, v151
	v_cvt_pk_fp8_f32 v114, v98, v102 op_sel:[0,0,1]
	v_mul_f32_e32 v102, s14, v115
	v_mul_f32_e32 v106, s13, v119
	v_med3_f32 v102, v102, s25, v151
	v_med3_f32 v106, v106, s25, v151
	v_mov_b32_e32 v110, 0
	v_cvt_pk_fp8_f32 v110, v102, v106
	v_mul_f32_e32 v98, s16, v127
	v_mul_f32_e32 v102, s15, v123
	v_med3_f32 v98, v98, s25, v151
	v_med3_f32 v102, v102, s25, v151
	v_cvt_pk_fp8_f32 v110, v98, v102 op_sel:[0,0,1]
	v_mul_f32_e32 v102, s10, v103
	v_med3_f32 v99, v99, s25, v151
	v_med3_f32 v102, v102, s25, v151
	v_mov_b32_e32 v103, 0
	v_cvt_pk_fp8_f32 v103, v99, v102
	v_mul_f32_e32 v98, s12, v111
	v_mul_f32_e32 v99, s0, v107
	v_med3_f32 v98, v98, s25, v151
	v_med3_f32 v99, v99, s25, v151
	v_cvt_pk_fp8_f32 v103, v98, v99 op_sel:[0,0,1]
	v_mul_f32_e32 v99, s14, v116
	v_mul_f32_e32 v102, s13, v120
	v_med3_f32 v99, v99, s25, v151
	v_med3_f32 v102, v102, s25, v151
	v_mov_b32_e32 v106, 0
	v_cvt_pk_fp8_f32 v106, v99, v102
	v_mul_f32_e32 v100, s11, v100
	v_mul_f32_e32 v102, s10, v104
	v_mul_f32_e32 v98, s16, v128
	v_mul_f32_e32 v99, s15, v124
	v_med3_f32 v100, v100, s25, v151
	v_med3_f32 v102, v102, s25, v151
	v_mov_b32_e32 v104, 0
	v_med3_f32 v98, v98, s25, v151
	v_med3_f32 v99, v99, s25, v151
	v_cvt_pk_fp8_f32 v104, v100, v102
	v_mul_f32_e32 v102, s14, v117
	v_mul_f32_e32 v107, s13, v121
; #define LAS __attribute__((address_space(3)))
; __device__ __forceinline__ void cvt8_pack(f32x4 (&v)[16], float gv, LAS unsigned char* lds, int sub, int wave, int lane) {
;     float gs[8];
; #pragma unroll
;     for (int i = 0; i < 8; ++i) gs[i] = __builtin_bit_cast(float, __builtin_amdgcn_readlane(__builtin_bit_cast(int, gv), i));
; #pragma unroll
;     for (int hf = 0; hf < 2; ++hf) { u32x4 w[2];
; #pragma unroll
;         for (int j = 0; j < 4; ++j) { const unsigned lo = pk4_fp8(v[0 + hf][j] * gs[0], v[2 + hf][j] * gs[1], v[4 + hf][j] * gs[2], v[6 + hf][j] * gs[3]), hi = pk4_fp8(v[8 + hf][j] * gs[4], v[10 + hf][j] * gs[5], v[12 + hf][j] * gs[6], v[14 + hf][j] * gs[7]);
;             if (j & 1) { w[j >> 1].z = lo; w[j >> 1].w = hi; } else { w[j >> 1].x = lo; w[j >> 1].y = hi; } }
;         const int sw = 8 * sub + 2 * (wave >> 1);
;         LAS unsigned char* p = lds + sub * 32768 + wave * 4096 + ((hf * 256 + 4 * lane) ^ (sw & 28)) * 8;
;         { const int o0 = 8 * (sw & 2), o1 = 16 - o0; const bool q = (lane >> 2) & 1;
;           *(LAS u32x4*)(p + (q ? o1 : o0)) = q ? w[1] : w[0]; *(LAS u32x4*)(p + (q ? o0 : o1)) = q ? w[0] : w[1]; } }
; }
; __device__ __forceinline__ void cvt8_phase(const Frame& F, const KArgs& a, const int bit, const int nb, const int s_lo, const int s_hi) {
;     ...
;     auto decode = [&](int s, int j) -> Cvt8Desc {
;         Cvt8Desc D;
;         if (s < S_WGU) { const int e = s / 64, rr = s % 64, kb4 = rr / 8, cb = rr % 8, kb = kb4 * 4 + j;
;             const int da = 4 * lane, db = 256 + 4 * lane;
;             D.W = a.in[20] + (size_t)e * DM * 2 * DFF; D.g = a.in[17]; D.ldw = 2 * DFF; D.k0 = kb * 64;
;             D.col0a = ((da & 255) < 128 ? 0 : DFF) + (cb * 2 + (da >> 8)) * 128 + (da & 127); D.col0b = ((db & 255) < 128 ? 0 : DFF) + (cb * 2 + (db >> 8)) * 128 + (db & 127);
;             D.dst = ws + WS_WGU + ((size_t)e * 2 * DFF + cb * 512) * DM + kb4 * 256; return D; }
;         s -= S_WGU;
;         { const int e = s / 32, rr = s % 32, kb4 = rr / 4, cb = rr % 4, kb = kb4 * 4 + j;
;             D.W = a.in[22] + (size_t)e * DFF * DM; D.g = nullptr; D.ldw = DM; D.k0 = kb * 64; D.col0a = cb * 512 + 4 * lane; D.col0b = cb * 512 + 256 + 4 * lane;
;             D.dst = ws + WS_WD + ((size_t)e * DM + cb * 512) * DFF + kb4 * 256; return D; }
;     };
	v_cvt_pk_fp8_f32 v106, v98, v99 op_sel:[0,0,1]
	v_mul_f32_e32 v99, s0, v108
	v_med3_f32 v102, v102, s25, v151
	v_med3_f32 v107, v107, s25, v151
	v_mov_b32_e32 v108, 0
	v_cvt_pk_fp8_f32 v108, v102, v107
	v_mul_f32_e32 v100, s16, v129
	v_mul_f32_e32 v102, s15, v125
	v_med3_f32 v100, v100, s25, v151
	v_med3_f32 v102, v102, s25, v151
	v_cvt_pk_fp8_f32 v108, v100, v102 op_sel:[0,0,1]
	v_mul_f32_e32 v101, s11, v101
	v_mul_f32_e32 v102, s10, v105
	v_med3_f32 v101, v101, s25, v151
	v_med3_f32 v102, v102, s25, v151
	v_mov_b32_e32 v105, 0
	v_cvt_pk_fp8_f32 v105, v101, v102
	v_mul_f32_e32 v98, s12, v112
	v_mul_f32_e32 v100, s12, v113
	v_mul_f32_e32 v101, s0, v109
	v_med3_f32 v98, v98, s25, v151
	v_med3_f32 v100, v100, s25, v151
	v_med3_f32 v101, v101, s25, v151
	v_med3_f32 v99, v99, s25, v151
	v_cvt_pk_fp8_f32 v105, v100, v101 op_sel:[0,0,1]
	v_cvt_pk_fp8_f32 v104, v98, v99 op_sel:[0,0,1]
	v_cndmask_b32_e64 v101, v108, v110, s[2:3]
	v_cndmask_b32_e64 v99, v106, v153, s[2:3]
	v_cndmask_b32_e64 v100, v105, v103, s[2:3]
	v_cndmask_b32_e64 v98, v104, v114, s[2:3]
	v_add_u32_e32 v102, v147, v137
	ds_write_b128 v102, v[98:101]
	v_cndmask_b32_e64 v101, v110, v108, s[2:3]
	v_cndmask_b32_e64 v100, v103, v105, s[2:3]
	v_cndmask_b32_e64 v99, v153, v106, s[2:3]
	v_cndmask_b32_e64 v98, v114, v104, s[2:3]
	v_add_u32_e32 v102, v147, v138
	v_mul_f32_e32 v85, s14, v85
	v_mul_f32_e32 v89, s13, v89
	ds_write_b128 v102, v[98:101]
	v_med3_f32 v85, v85, s25, v151
	v_med3_f32 v89, v89, s25, v151
	v_mov_b32_e32 v98, 0
	v_cvt_pk_fp8_f32 v98, v85, v89
	v_mul_f32_e32 v93, s16, v93
	v_mul_f32_e32 v89, s15, v97
	v_med3_f32 v85, v93, s25, v151
	v_med3_f32 v89, v89, s25, v151
	v_mul_f32_e32 v66, s11, v66
	v_mul_f32_e32 v70, s10, v70
	v_cvt_pk_fp8_f32 v98, v85, v89 op_sel:[0,0,1]
	v_med3_f32 v66, v66, s25, v151
	v_med3_f32 v70, v70, s25, v151
	v_mov_b32_e32 v85, 0
	v_cvt_pk_fp8_f32 v85, v66, v70
	v_mul_f32_e32 v78, s12, v78
	v_mul_f32_e32 v70, s0, v74
	v_med3_f32 v66, v78, s25, v151
	v_med3_f32 v70, v70, s25, v151
	v_cvt_pk_fp8_f32 v85, v66, v70 op_sel:[0,0,1]
	v_mul_f32_e32 v70, s14, v82
	v_mul_f32_e32 v74, s13, v86
	v_med3_f32 v70, v70, s25, v151
	v_med3_f32 v74, v74, s25, v151
	v_mov_b32_e32 v78, 0
	v_cvt_pk_fp8_f32 v78, v70, v74
	v_mul_f32_e32 v66, s16, v90
	v_mul_f32_e32 v70, s15, v94
	v_med3_f32 v66, v66, s25, v151
	v_med3_f32 v70, v70, s25, v151
	v_cvt_pk_fp8_f32 v78, v66, v70 op_sel:[0,0,1]
	v_mul_f32_e32 v67, s11, v67
	v_mul_f32_e32 v70, s10, v71
	v_med3_f32 v67, v67, s25, v151
	v_med3_f32 v70, v70, s25, v151
	v_mov_b32_e32 v71, 0
	v_cvt_pk_fp8_f32 v71, v67, v70
	v_mul_f32_e32 v66, s12, v79
	v_mul_f32_e32 v67, s0, v75
	v_med3_f32 v66, v66, s25, v151
	v_med3_f32 v67, v67, s25, v151
	v_cvt_pk_fp8_f32 v71, v66, v67 op_sel:[0,0,1]
	v_mul_f32_e32 v67, s14, v83
	v_mul_f32_e32 v70, s13, v87
	v_med3_f32 v67, v67, s25, v151
	v_med3_f32 v70, v70, s25, v151
	v_mov_b32_e32 v74, 0
	v_cvt_pk_fp8_f32 v74, v67, v70
	v_mul_f32_e32 v66, s16, v91
	v_mul_f32_e32 v67, s15, v95
	v_med3_f32 v66, v66, s25, v151
	v_med3_f32 v67, v67, s25, v151
	v_cvt_pk_fp8_f32 v74, v66, v67 op_sel:[0,0,1]
	v_mul_f32_e32 v67, s0, v76
	v_mul_f32_e32 v75, s14, v84
	v_mul_f32_e32 v76, s13, v88
	v_mul_f32_e32 v68, s11, v68
	v_mul_f32_e32 v70, s10, v72
	v_med3_f32 v75, v75, s25, v151
	v_med3_f32 v76, v76, s25, v151
	v_mov_b32_e32 v79, 0
	v_mul_f32_e32 v69, s11, v69
	v_mul_f32_e32 v73, s10, v73
	v_med3_f32 v68, v68, s25, v151
	v_med3_f32 v70, v70, s25, v151
	v_mov_b32_e32 v72, 0
	v_cvt_pk_fp8_f32 v79, v75, v76
	v_med3_f32 v69, v69, s25, v151
	v_med3_f32 v73, v73, s25, v151
	v_mov_b32_e32 v76, 0
	v_cvt_pk_fp8_f32 v72, v68, v70
	v_cvt_pk_fp8_f32 v76, v69, v73
	v_mul_f32_e32 v66, s12, v80
	v_mul_f32_e32 v68, s16, v92
	v_mul_f32_e32 v70, s15, v96
	v_mul_f32_e32 v75, s12, v81
	v_mul_f32_e32 v73, s0, v77
	v_med3_f32 v66, v66, s25, v151
	v_med3_f32 v67, v67, s25, v151
	v_med3_f32 v68, v68, s25, v151
	v_med3_f32 v70, v70, s25, v151
	v_med3_f32 v69, v75, s25, v151
	v_med3_f32 v73, v73, s25, v151
	v_cvt_pk_fp8_f32 v76, v69, v73 op_sel:[0,0,1]
	v_cvt_pk_fp8_f32 v79, v68, v70 op_sel:[0,0,1]
	v_cvt_pk_fp8_f32 v72, v66, v67 op_sel:[0,0,1]
	v_cndmask_b32_e64 v69, v98, v74, s[2:3]
	v_cndmask_b32_e64 v68, v76, v71, s[2:3]
	v_cndmask_b32_e64 v67, v79, v78, s[2:3]
	v_cndmask_b32_e64 v66, v72, v85, s[2:3]
	v_add_u32_e32 v70, v148, v137
	ds_write_b128 v70, v[66:69]
	v_cndmask_b32_e64 v69, v74, v98, s[2:3]
	v_cndmask_b32_e64 v68, v71, v76, s[2:3]
	v_cndmask_b32_e64 v67, v78, v79, s[2:3]
	v_cndmask_b32_e64 v66, v85, v72, s[2:3]
	v_add_u32_e32 v70, v148, v138
	s_mov_b64 s[10:11], -1
	s_and_b64 vcc, exec, s[6:7]
	ds_write_b128 v70, v[66:69]
	s_cbranch_vccz .LBB0_1137
	s_add_i32 s0, s19, 0xfffff800
	s_lshl_b32 s6, s19, 6
	s_lshr_b32 s0, s0, 5
	s_and_b32 s10, s6, 0x700
	s_lshl_b32 s6, s19, 20
	s_and_b32 s11, s6, 0x300000
	s_lshl_b64 s[6:7], s[0:1], 22
	s_add_u32 s0, s20, s6
	s_addc_u32 s6, s21, s7
	s_add_u32 s0, s0, s11
	s_addc_u32 s7, s6, 0
	s_add_u32 s6, s0, s10
	s_addc_u32 s7, s7, 0
	s_mov_b64 s[10:11], 0
